# w2 expert-weight fp8 conversion moved out of P15 into P17: 32 dedicated converter WGs (4 per XCD) run beside the 224-WG expert gate/up GEMM
# speedup vs baseline: 1.0529x; 1.0529x over previous
.LBB0_168:
	global_load_dwordx4 v[94:97], v[104:105], off offset:-4096
	global_load_dwordx4 v[90:93], v[104:105], off offset:-3072
	global_load_dwordx4 v[86:89], v[104:105], off offset:-2048
	global_load_dwordx4 v[82:85], v[104:105], off offset:-1024
	global_load_dwordx4 v[78:81], v[104:105], off
	global_load_dwordx4 v[74:77], v[104:105], off offset:1024
	global_load_dwordx4 v[70:73], v[104:105], off offset:2048
	global_load_dwordx4 v[66:69], v[104:105], off offset:3072
	s_cmp_lt_i32 s75, 0xe000
	s_cselect_b64 s[22:23], -1, 0
	s_cmp_gt_i32 s75, 0xdfff
	s_cbranch_scc1 .LBB0_173
	s_cmp_gt_i32 s75, 0xdfff
	s_mov_b64 s[2:3], -1
	s_cbranch_scc0 .LBB0_171
	s_add_i32 s2, s75, 0x2000
	s_bfe_u32 s3, s2, 0x70009
	s_mulk_i32 s3, 0x2493
	s_lshr_b32 s21, s3, 16
	s_mul_i32 s3, s21, 0xe00
	s_sub_i32 s2, s2, s3
	v_readlane_b32 s36, v250, 32
	s_and_b32 s8, s2, 0xffff
	s_mul_i32 s2, s21, 0x3800000
	v_readlane_b32 s42, v250, 38
	v_readlane_b32 s43, v250, 39
	s_add_u32 s2, s42, s2
	s_addc_u32 s3, s43, 0
	s_lshl_b32 s20, s8, 1
	s_and_b32 s20, s20, 0x1f80
	v_or_b32_e32 v2, s20, v98
	v_lshlrev_b32_e32 v102, 13, v2
	v_lshl_add_u64 v[2:3], s[2:3], 0, v[102:103]
	s_lshl_b32 s2, s8, 5
	s_and_b32 s2, s2, 0x7e0
	s_lshl_b32 s3, s21, 11
	s_lshl_b32 s8, s2, 2
	s_or_b32 s2, s3, s2
	v_or_b32_e32 v6, s2, v100
	v_mov_b64_e32 v[4:5], s[10:11]
	v_mad_u64_u32 v[4:5], s[2:3], v6, s7, v[4:5]
	s_mov_b32 s21, s9
	v_readlane_b32 s37, v250, 33
	v_readlane_b32 s38, v250, 34
	v_readlane_b32 s39, v250, 35
	v_readlane_b32 s40, v250, 36
	v_readlane_b32 s41, v250, 37
	v_lshl_add_u64 v[2:3], v[2:3], 0, s[8:9]
	v_lshl_add_u64 v[108:109], v[4:5], 0, s[20:21]
	s_mov_b64 s[2:3], 0

.LBB0_251:
	v_readlane_b32 s0, v250, 44
	v_readlane_b32 s1, v250, 45
	s_andn2_b64 vcc, exec, s[0:1]
	s_cbranch_vccnz .LBB0_285
	s_abs_i32 s0, s97
	v_cvt_f32_u32_e32 v1, s0
	s_sub_i32 s5, 0, s0
	s_add_i32 s1, s97, 0x21f
	s_xor_b32 s4, s1, s97
	v_rcp_iflag_f32_e32 v1, v1
	s_abs_i32 s1, s1
	s_ashr_i32 s4, s4, 31
	v_mul_f32_e32 v1, 0x4f7ffffe, v1
	v_cvt_u32_f32_e32 v1, v1
	s_nop 0
	v_readfirstlane_b32 s6, v1
	s_mul_i32 s5, s5, s6
	s_mul_hi_u32 s5, s6, s5
	s_add_i32 s6, s6, s5
	s_mul_hi_u32 s5, s1, s6
	s_mul_i32 s6, s5, s0
	s_sub_i32 s1, s1, s6
	s_add_i32 s7, s5, 1
	s_sub_i32 s6, s1, s0
	s_cmp_ge_u32 s1, s0
	s_cselect_b32 s5, s7, s5
	s_cselect_b32 s1, s6, s1
	s_add_i32 s6, s5, 1
	s_cmp_ge_u32 s1, s0
	s_cselect_b32 s0, s6, s5
	s_not_b32 s1, s4
	s_xor_b32 s0, s0, s4
	s_add_i32 s0, s1, s0
	s_mul_i32 s0, s0, s97
	s_sub_i32 s4, 0x220, s0
	s_cmp_ge_i32 s4, s97
	s_cselect_b64 s[0:1], -1, 0
	s_cmp_lt_i32 s74, s4
	s_cselect_b64 s[4:5], -1, 0
	s_or_b64 s[0:1], s[0:1], s[4:5]
	s_and_b64 vcc, exec, s[0:1]
	s_cbranch_vccnz .LBB0_285
	s_cmp_gt_i32 s75, 0xdfff
	s_cbranch_scc1 .LBB0_285
	v_readlane_b32 s0, v250, 55
	v_and_b32_e32 v2, 7, v0
	v_lshrrev_b32_e32 v3, 3, v178
	s_xor_b32 s14, s0, 0x80000000
	s_cmp_gt_i32 s75, 0xdfff
	v_lshlrev_b32_e32 v1, 4, v3
	v_lshlrev_b32_e32 v134, 2, v2
	v_lshlrev_b32_e32 v2, 4, v2
	s_cbranch_scc0 .LBB0_256
	s_add_i32 s0, s75, 0x2000
	s_bfe_u32 s1, s0, 0x70009
	s_mulk_i32 s1, 0x2493
	s_lshr_b32 s7, s1, 16
	s_mul_i32 s1, s7, 0xe00
	s_sub_i32 s0, s0, s1
	v_readlane_b32 s16, v250, 32
	s_and_b32 s0, s0, 0xffff
	s_mul_i32 s4, s7, 0x3800000
	v_readlane_b32 s22, v250, 38
	v_readlane_b32 s23, v250, 39
	s_add_u32 s4, s22, s4
	s_addc_u32 s5, s23, 0
	s_lshl_b32 s6, s0, 1
	s_and_b32 s6, s6, 0x1f80
	v_lshlrev_b32_e32 v136, 4, v3
	v_or_b32_e32 v3, s6, v136
	v_lshlrev_b32_e32 v4, 13, v3
	v_mov_b32_e32 v5, 0
	s_lshl_b32 s0, s0, 5
	v_lshl_add_u64 v[6:7], s[4:5], 0, v[4:5]
	s_and_b32 s4, s0, 0x7e0
	s_mov_b32 s1, 0
	s_lshl_b32 s0, s4, 2
	v_lshl_add_u64 v[6:7], v[6:7], 0, s[0:1]
	s_lshl_b32 s0, s7, 11
	v_mov_b32_e32 v3, v5
	s_or_b32 s0, s0, s4
	v_mov_b32_e32 v135, v5
	v_lshl_add_u64 v[6:7], v[6:7], 0, v[2:3]
	v_or_b32_e32 v3, s0, v134
	s_movk_i32 s0, 0x1c00
	v_mov_b64_e32 v[4:5], s[78:79]
	v_mad_u64_u32 v[4:5], s[4:5], v3, s0, v[4:5]
	s_mov_b32 s7, s1
	v_lshl_add_u64 v[4:5], v[4:5], 0, s[6:7]
	s_mov_b64 s[0:1], 0x24500000
	v_readlane_b32 s17, v250, 33
	v_readlane_b32 s18, v250, 34
	v_readlane_b32 s19, v250, 35
	v_readlane_b32 s20, v250, 36
	v_readlane_b32 s21, v250, 37
	v_lshl_add_u64 v[66:67], v[4:5], 0, s[0:1]
	s_mov_b64 s[0:1], 0
	s_mov_b32 s15, 0x43000000
	s_branch .LBB0_257

.LBB0_262:
	s_cmp_gt_i32 s17, 0
	s_cselect_b64 s[0:1], -1, 0
	s_cmp_lt_i32 s75, 0xe000
	s_cselect_b64 s[12:13], -1, 0
	s_and_b64 s[12:13], s[0:1], s[12:13]
	v_cndmask_b32_e64 v130, 0, 1, s[12:13]
	v_cmp_ne_u32_e64 s[0:1], 1, v130
	s_andn2_b64 vcc, exec, s[12:13]
	s_cbranch_vccnz .LBB0_269
	s_cmp_gt_i32 s75, 0xdfff
	s_mov_b64 s[10:11], -1
	s_cbranch_scc0 .LBB0_265
	s_add_i32 s10, s75, 0x2000
	s_bfe_u32 s11, s10, 0x70009
	s_mulk_i32 s11, 0x2493
	s_lshr_b32 s13, s11, 16
	s_mul_i32 s11, s13, 0xe00
	s_sub_i32 s10, s10, s11
	v_readlane_b32 s24, v250, 32
	s_and_b32 s21, s10, 0xffff
	s_mul_i32 s10, s13, 0x3800000
	v_readlane_b32 s30, v250, 38
	v_readlane_b32 s31, v250, 39
	s_add_u32 s10, s30, s10
	s_addc_u32 s11, s31, 0
	s_lshl_b32 s12, s21, 1
	s_and_b32 s12, s12, 0x1f80
	s_waitcnt vmcnt(16)
	v_or_b32_e32 v66, s12, v136
	v_lshlrev_b32_e32 v138, 13, v66
	v_lshl_add_u64 v[66:67], s[10:11], 0, v[138:139]
	s_lshl_b32 s10, s21, 5
	s_and_b32 s21, s10, 0x7e0
	s_lshl_b32 s10, s21, 2
	s_mov_b32 s11, s5
	v_lshl_add_u64 v[66:67], v[66:67], 0, s[10:11]
	s_lshl_b32 s10, s13, 11
	s_or_b32 s10, s10, s21
	v_or_b32_e32 v68, s10, v134
	v_mul_hi_i32_i24_e32 v69, 0x1c00, v68
	v_mul_i32_i24_e32 v68, 0x1c00, v68
	v_lshl_add_u64 v[68:69], s[6:7], 0, v[68:69]
	s_mov_b32 s13, s5
	v_readlane_b32 s25, v250, 33
	v_readlane_b32 s26, v250, 34
	v_readlane_b32 s27, v250, 35
	v_readlane_b32 s28, v250, 36
	v_readlane_b32 s29, v250, 37
	v_lshl_add_u64 v[130:131], v[68:69], 0, s[12:13]
	s_mov_b64 s[10:11], 0

.LBB0_273:
	v_mad_u64_u32 v[144:145], s[12:13], s4, 3, v[140:141]
	s_and_b64 vcc, exec, s[0:1]
	s_mov_b64 s[0:1], 0
	global_store_dwordx4 v[144:145], v[130:133], off
	s_cbranch_vccnz .LBB0_261
	s_cmp_gt_i32 s17, 0
	s_cselect_b64 s[0:1], -1, 0
	s_cmp_lt_i32 s75, 0xe000
	s_cselect_b64 s[12:13], -1, 0
	s_and_b64 s[0:1], s[0:1], s[12:13]
	s_andn2_b64 vcc, exec, s[0:1]
	s_cbranch_vccnz .LBB0_281
	s_cmp_gt_i32 s75, 0xdfff
	s_mov_b64 s[12:13], -1
	s_cbranch_scc0 .LBB0_277
	s_add_i32 s4, s75, 0x2000
	s_bfe_u32 s11, s4, 0x70009
	s_mulk_i32 s11, 0x2493
	s_lshr_b32 s11, s11, 16
	s_mul_i32 s12, s11, 0xe00
	s_sub_i32 s4, s4, s12
	v_readlane_b32 s24, v250, 32
	s_and_b32 s4, s4, 0xffff
	s_mul_i32 s12, s11, 0x3800000
	v_readlane_b32 s30, v250, 38
	v_readlane_b32 s31, v250, 39
	s_add_u32 s12, s30, s12
	s_addc_u32 s13, s31, 0
	s_lshl_b32 s15, s4, 1
	s_and_b32 s22, s15, 0x1f80
	s_waitcnt vmcnt(16)
	v_or_b32_e32 v2, s22, v136
	v_lshlrev_b32_e32 v138, 13, v2
	s_lshl_b32 s4, s4, 5
	v_lshl_add_u64 v[2:3], s[12:13], 0, v[138:139]
	s_and_b32 s12, s4, 0x7e0
	s_lshl_b32 s4, s12, 2
	v_lshl_add_u64 v[2:3], v[2:3], 0, s[4:5]
	s_lshl_b32 s4, s11, 11
	s_or_b32 s4, s4, s12
	v_or_b32_e32 v4, s4, v134
	v_mul_hi_i32_i24_e32 v5, 0x1c00, v4
	v_mul_i32_i24_e32 v4, 0x1c00, v4
	v_lshl_add_u64 v[4:5], s[6:7], 0, v[4:5]
	s_mov_b32 s23, s5
	v_readlane_b32 s25, v250, 33
	v_readlane_b32 s26, v250, 34
	v_readlane_b32 s27, v250, 35
	v_readlane_b32 s28, v250, 36
	v_readlane_b32 s29, v250, 37
	v_lshl_add_u64 v[130:131], v[4:5], 0, s[22:23]
	s_mov_b64 s[12:13], 0

.LBB0_346:
	v_writelane_b32 v253, s2, 41
	s_lshl_b32 s2, s81, 4
	s_add_i32 s28, s2, s49
	v_or_b32_e32 v4, s28, v124
	v_mov_b64_e32 v[2:3], s[4:5]
	v_mad_u64_u32 v[4:5], s[2:3], v4, s6, v[2:3]
	v_lshl_add_u64 v[4:5], v[4:5], 0, v[108:109]
	v_or_b32_e32 v107, s28, v101
	v_lshl_add_u64 v[4:5], v[4:5], 0, v[112:113]
	s_mov_b64 s[2:3], 0x1800
	v_lshl_add_u64 v[6:7], v[4:5], 0, s[2:3]
	v_add_co_u32_e32 v4, vcc, 0x1000, v4
	v_mad_u64_u32 v[2:3], s[2:3], v107, s6, v[2:3]
	s_nop 0
	v_addc_co_u32_e32 v5, vcc, 0, v5, vcc
	s_mov_b64 s[2:3], 0x2080
	global_load_dwordx4 v[18:21], v[6:7], off offset:32
	global_load_dwordx4 v[22:25], v[6:7], off offset:64
	global_load_dwordx4 v[26:29], v[4:5], off offset:2048
	global_load_dwordx4 v[30:33], v[6:7], off offset:96
	v_lshl_add_u64 v[4:5], v[2:3], 0, s[2:3]
	v_add_co_u32_e32 v2, vcc, 0x2000, v2
	v_writelane_b32 v253, s4, 43
	s_nop 0
	v_addc_co_u32_e32 v3, vcc, 0, v3, vcc
	global_load_dwordx4 v[6:9], v[2:3], off offset:128
	s_nop 0
	global_load_dwordx4 v[2:5], v[4:5], off offset:16
	s_cmp_gt_i32 s75, 0xdfff
	v_writelane_b32 v253, s5, 44
	s_cbranch_scc1 .LBB0_357
	s_cmp_gt_i32 s75, 0xdfff
	s_mov_b64 s[2:3], -1
	s_cbranch_scc0 .LBB0_349
	s_add_i32 s2, s75, 0x2000
	s_bfe_u32 s3, s2, 0x70009
	s_mulk_i32 s3, 0x2493
	s_lshr_b32 s5, s3, 16
	s_mul_i32 s3, s5, 0xe00
	s_sub_i32 s2, s2, s3
	s_and_b32 s6, s2, 0xffff
	s_mul_i32 s2, s5, 0x3800000
	s_add_u32 s2, s22, s2
	s_addc_u32 s3, s23, 0
	s_lshl_b32 s4, s6, 1
	s_and_b32 s4, s4, 0x1f80
	v_or_b32_e32 v10, s4, v98
	v_lshlrev_b32_e32 v96, 13, v10
	v_lshl_add_u64 v[10:11], s[2:3], 0, v[96:97]
	s_lshl_b32 s2, s6, 5
	s_and_b32 s2, s2, 0x7e0
	s_lshl_b32 s3, s5, 11
	s_lshl_b32 s68, s2, 2
	s_or_b32 s2, s3, s2
	v_or_b32_e32 v14, s2, v100
	v_readlane_b32 s2, v251, 22
	v_readlane_b32 s3, v251, 23
	s_mov_b32 s5, s69
	v_lshl_add_u64 v[10:11], v[10:11], 0, s[68:69]
	v_mov_b64_e32 v[12:13], s[2:3]
	s_movk_i32 s2, 0x1c00
	v_mad_u64_u32 v[12:13], s[2:3], v14, s2, v[12:13]
	v_lshl_add_u64 v[90:91], v[12:13], 0, s[4:5]
	s_mov_b64 s[2:3], 0

.LBB0_369:
	s_cmp_lt_i32 s75, 0xe000
	s_cselect_b64 s[8:9], -1, 0
	s_and_b64 vcc, exec, s[8:9]
	v_writelane_b32 v253, s75, 45
	s_cbranch_vccz .LBB0_374
	s_cmp_gt_i32 s75, 0xdfff
	s_mov_b64 s[0:1], -1
	s_cbranch_scc0 .LBB0_372
	s_add_i32 s0, s75, 0x2000
	s_bfe_u32 s1, s0, 0x70009
	s_mulk_i32 s1, 0x2493
	s_lshr_b32 s3, s1, 16
	s_mul_i32 s1, s3, 0xe00
	s_sub_i32 s0, s0, s1
	s_and_b32 s4, s0, 0xffff
	s_mul_i32 s0, s3, 0x3800000
	s_add_u32 s0, s22, s0
	s_addc_u32 s1, s23, 0
	s_lshl_b32 s2, s4, 1
	s_and_b32 s2, s2, 0x1f80
	v_or_b32_e32 v2, s2, v98
	v_lshlrev_b32_e32 v96, 13, v2
	v_lshl_add_u64 v[2:3], s[0:1], 0, v[96:97]
	s_lshl_b32 s0, s4, 5
	s_and_b32 s0, s0, 0x7e0
	s_lshl_b32 s1, s3, 11
	s_lshl_b32 s68, s0, 2
	s_or_b32 s0, s1, s0
	v_or_b32_e32 v6, s0, v100
	v_readlane_b32 s0, v251, 22
	v_readlane_b32 s1, v251, 23
	s_mov_b32 s3, s69
	v_lshl_add_u64 v[2:3], v[2:3], 0, s[68:69]
	v_mov_b64_e32 v[4:5], s[0:1]
	s_movk_i32 s0, 0x1c00
	v_mad_u64_u32 v[4:5], s[0:1], v6, s0, v[4:5]
	v_lshl_add_u64 v[66:67], v[4:5], 0, s[2:3]
	s_mov_b64 s[0:1], 0

.LBB0_394:
	v_writelane_b32 v253, s28, 51
	s_waitcnt vmcnt(0)
	v_mov_b32_e32 v2, s39
	v_mov_b32_e32 v3, s37
	v_writelane_b32 v253, s29, 52
	v_writelane_b32 v253, s26, 53
	v_readlane_b32 s70, v252, 56
	v_readlane_b32 s71, v252, 57
	v_writelane_b32 v253, s27, 54
	v_writelane_b32 v253, s68, 55
	v_readlane_b32 s74, v252, 54
	v_readlane_b32 s75, v252, 55
	v_writelane_b32 v253, s69, 56
	s_mov_b64 vcc, s[18:19]
	v_readlane_b32 s40, v253, 30
	v_readlane_b32 s41, v253, 31
	v_writelane_b32 v253, s38, 57
	v_readlane_b32 s18, v252, 52
	v_cndmask_b32_e64 v2, 0, v2, s[40:41]
	v_writelane_b32 v253, s39, 58
	v_readlane_b32 s19, v252, 53
	v_readlane_b32 s38, v253, 28
	v_readlane_b32 s39, v253, 29
	v_writelane_b32 v253, s36, 59
	s_mov_b32 s52, s86
	v_cndmask_b32_e64 v2, v2, v3, s[38:39]
	v_writelane_b32 v253, s37, 60
	v_mov_b32_e32 v3, s35
	v_readlane_b32 s36, v253, 26
	v_readlane_b32 s37, v253, 27
	v_writelane_b32 v253, s34, 61
	v_readlane_b32 s84, v252, 46
	v_cndmask_b32_e64 v2, v2, v3, s[36:37]
	v_writelane_b32 v253, s35, 62
	v_mov_b32_e32 v3, s97
	v_readlane_b32 s34, v253, 24
	v_readlane_b32 s35, v253, 25
	v_readlane_b32 s85, v252, 47
	s_mov_b32 s80, s72
	v_cndmask_b32_e64 v2, v2, v3, s[34:35]
	v_mov_b32_e32 v3, s31
	v_writelane_b32 v253, s30, 63
	s_mov_b64 s[76:77], s[94:95]
	v_readlane_b32 s28, v253, 20
	v_writelane_b32 v254, s31, 0
	v_readlane_b32 s30, v253, 22
	v_readlane_b32 s31, v253, 23
	v_readlane_b32 s29, v253, 21
	v_readlane_b32 s26, v253, 18
	v_cndmask_b32_e64 v2, v2, v3, s[30:31]
	v_mov_b32_e32 v3, s51
	v_cndmask_b32_e64 v2, v2, v3, s[28:29]
	v_mov_b32_e32 v3, s91
	v_readlane_b32 s27, v253, 19
	v_readlane_b32 s0, v253, 10
	v_readlane_b32 s1, v253, 11
	v_cndmask_b32_e64 v2, v2, v3, s[26:27]
	v_mov_b32_e32 v3, s25
	v_writelane_b32 v254, s24, 1
	v_readlane_b32 s14, v253, 6
	v_readlane_b32 s15, v253, 7
	v_writelane_b32 v254, s25, 2
	v_readlane_b32 s24, v253, 16
	v_readlane_b32 s25, v253, 17
	v_readlane_b32 s8, v253, 0
	v_readlane_b32 s9, v253, 1
	v_cndmask_b32_e64 v2, v2, v3, s[24:25]
	v_mov_b32_e32 v3, s23
	v_writelane_b32 v254, s22, 3
	v_readlane_b32 s68, v252, 42
	v_readlane_b32 s69, v252, 43
	v_writelane_b32 v254, s23, 4
	v_readlane_b32 s22, v253, 14
	v_readlane_b32 s23, v253, 15
	v_readlane_b32 s92, v252, 40
	v_readlane_b32 s93, v252, 41
	v_cndmask_b32_e64 v2, v2, v3, s[22:23]
	v_mov_b32_e32 v3, s21
	v_writelane_b32 v254, s20, 5
	v_readlane_b32 s94, v252, 38
	v_readlane_b32 s95, v252, 39
	v_writelane_b32 v254, s21, 6
	v_readlane_b32 s20, v253, 12
	v_readlane_b32 s21, v253, 13
	v_readlane_b32 s66, v252, 36
	v_readlane_b32 s67, v252, 37
	v_cndmask_b32_e64 v2, v2, v3, s[20:21]
	v_mov_b32_e32 v3, s89
	v_cndmask_b32_e64 v2, v2, v3, s[0:1]
	v_mov_b32_e32 v3, s17
	v_writelane_b32 v254, s16, 7
	s_mov_b32 s48, s82
	v_readlane_b32 s78, v253, 57
	v_writelane_b32 v254, s17, 8
	v_readlane_b32 s16, v253, 8
	v_readlane_b32 s17, v253, 9
	v_lshlrev_b32_e32 v122, 2, v178
	v_mov_b32_e32 v107, v97
	v_cndmask_b32_e64 v2, v2, v3, s[16:17]
	v_mov_b32_e32 v3, s87
	v_cndmask_b32_e64 v2, v2, v3, s[14:15]
	v_mov_b32_e32 v3, s13
	v_writelane_b32 v254, s12, 9
	v_readlane_b32 s86, v252, 48
	v_readlane_b32 s87, v252, 49
	v_writelane_b32 v254, s13, 10
	v_readlane_b32 s12, v253, 4
	v_readlane_b32 s13, v253, 5
	v_mov_b32_e32 v111, v97
	v_readlane_b32 s79, v253, 58
	v_cndmask_b32_e64 v2, v2, v3, s[12:13]
	v_mov_b32_e32 v3, s11
	v_writelane_b32 v254, s10, 11
	s_nop 1
	v_writelane_b32 v254, s11, 12
	v_readlane_b32 s10, v253, 2
	v_readlane_b32 s11, v253, 3
	s_nop 1
	v_cndmask_b32_e64 v2, v2, v3, s[10:11]
	v_mov_b32_e32 v3, s45
	v_cndmask_b32_e64 v2, v2, v3, s[8:9]
	v_mov_b32_e32 v3, s7
	v_writelane_b32 v254, s6, 13
	s_nop 1
	v_writelane_b32 v254, s7, 14
	v_readlane_b32 s6, v252, 62
	v_readlane_b32 s7, v252, 63
	s_nop 1
	v_cndmask_b32_e64 v2, v2, v3, s[6:7]
	v_mov_b32_e32 v3, s5
	v_writelane_b32 v254, s4, 15
	s_nop 1
	v_writelane_b32 v254, s5, 16
	v_readlane_b32 s4, v252, 60
	v_writelane_b32 v254, s44, 17
	v_readlane_b32 s5, v252, 61
	s_nop 0
	v_writelane_b32 v254, s45, 18
	v_cndmask_b32_e64 v2, v2, v3, s[4:5]
	v_mov_b32_e32 v3, s3
	v_writelane_b32 v254, s2, 19
	s_mov_b32 s44, s88
	v_readlane_b32 s88, v252, 50
	v_writelane_b32 v254, s3, 20
	v_readlane_b32 s2, v252, 58
	v_readlane_b32 s3, v252, 59
	v_readlane_b32 s89, v252, 51
	v_writelane_b32 v254, s42, 21
	v_cndmask_b32_e64 v2, v2, v3, s[2:3]
	v_mov_b32_e32 v3, s83
	v_cndmask_b32_e64 v2, v2, v3, s[70:71]
	v_mov_b32_e32 v3, s73
	v_cndmask_b32_e64 v2, v2, v3, s[74:75]
	v_mov_b32_e32 v3, vcc_hi
	v_cndmask_b32_e64 v2, v2, v3, s[18:19]
	v_mov_b32_e32 v3, s63
	v_cndmask_b32_e64 v2, v2, v3, s[88:89]
	v_mov_b32_e32 v3, s61
	v_cndmask_b32_e64 v2, v2, v3, s[86:87]
	v_mov_b32_e32 v3, s59
	v_readlane_b32 s72, v252, 44
	v_cndmask_b32_e64 v2, v2, v3, s[84:85]
	v_mov_b32_e32 v3, s57
	v_readlane_b32 s73, v252, 45
	v_writelane_b32 v254, s43, 22
	v_readlane_b32 s82, v252, 34
	v_cndmask_b32_e64 v2, v2, v3, s[72:73]
	v_mov_b32_e32 v3, s77
	v_cndmask_b32_e64 v2, v2, v3, s[68:69]
	v_mov_b32_e32 v3, s43
	v_cndmask_b32_e64 v2, v2, v3, s[92:93]
	v_mov_b32_e32 v3, s65
	v_cndmask_b32_e64 v2, v2, v3, s[94:95]
	v_mov_b32_e32 v3, s55
	v_writelane_b32 v254, s54, 23
	v_cndmask_b32_e64 v2, v2, v3, s[66:67]
	v_mov_b32_e32 v3, s47
	v_writelane_b32 v254, s55, 24
	v_writelane_b32 v254, s64, 25
	v_readlane_b32 s83, v252, 35
	v_readlane_b32 s54, v253, 49
	v_writelane_b32 v254, s65, 26
	v_writelane_b32 v254, s46, 27
	s_mov_b32 s64, vcc_lo
	v_readlane_b32 vcc_lo, v252, 32
	v_writelane_b32 v254, s47, 28
	v_readlane_b32 s46, v253, 47
	v_readlane_b32 s47, v253, 48
	v_cndmask_b32_e64 v2, v2, v3, s[82:83]
	v_readlane_b32 vcc_hi, v252, 33
	v_mov_b32_e32 v3, s47
	s_mov_b32 s42, s76
	v_readlane_b32 s55, v253, 50
	v_readlane_b32 s76, v252, 23
	v_cndmask_b32_e32 v2, v2, v3, vcc
	v_mov_b32_e32 v3, s55
	v_readlane_b32 s77, v252, 24
	s_nop 1
	v_cndmask_b32_e64 v2, v2, v3, s[76:77]
	v_mov_b32_e32 v3, s78
	v_cndmask_b32_e64 v3, 0, v3, s[40:41]
	v_readlane_b32 s40, v253, 59
	v_readlane_b32 s41, v253, 60
	s_nop 0
	v_mov_b32_e32 v4, s40
	v_cndmask_b32_e64 v3, v3, v4, s[38:39]
	v_readlane_b32 s38, v253, 61
	v_readlane_b32 s39, v253, 62
	s_nop 0
	v_mov_b32_e32 v4, s38
	v_cndmask_b32_e64 v3, v3, v4, s[36:37]
	v_mov_b32_e32 v4, s96
	v_cndmask_b32_e64 v3, v3, v4, s[34:35]
	v_readlane_b32 s34, v253, 63
	v_readlane_b32 s35, v254, 0
	s_nop 0
	v_mov_b32_e32 v4, s34
	v_cndmask_b32_e64 v3, v3, v4, s[30:31]
	v_mov_b32_e32 v4, s50
	v_cndmask_b32_e64 v3, v3, v4, s[28:29]
	v_mov_b32_e32 v4, s90
	v_cndmask_b32_e64 v3, v3, v4, s[26:27]
	v_readlane_b32 s26, v254, 1
	v_readlane_b32 s27, v254, 2
	s_nop 0
	v_mov_b32_e32 v4, s26
	v_cndmask_b32_e64 v3, v3, v4, s[24:25]
	v_readlane_b32 s24, v254, 3
	v_readlane_b32 s25, v254, 4
	s_nop 0
	v_mov_b32_e32 v4, s24
	v_cndmask_b32_e64 v3, v3, v4, s[22:23]
	v_readlane_b32 s22, v254, 5
	v_readlane_b32 s23, v254, 6
	s_nop 0
	v_mov_b32_e32 v4, s22
	v_cndmask_b32_e64 v3, v3, v4, s[20:21]
	v_mov_b32_e32 v4, s44
	v_cndmask_b32_e64 v3, v3, v4, s[0:1]
	v_readlane_b32 s0, v254, 7
	v_readlane_b32 s1, v254, 8
	s_nop 0
	v_mov_b32_e32 v4, s0
	v_readlane_b32 s0, v254, 9
	v_cndmask_b32_e64 v3, v3, v4, s[16:17]
	v_mov_b32_e32 v4, s52
	v_readlane_b32 s1, v254, 10
	v_cndmask_b32_e64 v3, v3, v4, s[14:15]
	v_mov_b32_e32 v4, s0
	v_readlane_b32 s0, v254, 11
	v_readlane_b32 s1, v254, 12
	v_cndmask_b32_e64 v3, v3, v4, s[12:13]
	v_mov_b32_e32 v4, s0
	v_readlane_b32 s0, v254, 17
	v_readlane_b32 s1, v254, 18
	v_cndmask_b32_e64 v3, v3, v4, s[10:11]
	v_mov_b32_e32 v4, s0
	v_readlane_b32 s0, v254, 13
	v_readlane_b32 s1, v254, 14
	v_cndmask_b32_e64 v3, v3, v4, s[8:9]
	v_mov_b32_e32 v4, s0
	v_readlane_b32 s0, v254, 15
	v_readlane_b32 s1, v254, 16
	v_cndmask_b32_e64 v3, v3, v4, s[6:7]
	v_mov_b32_e32 v4, s0
	v_readlane_b32 s0, v254, 19
	v_cndmask_b32_e64 v3, v3, v4, s[4:5]
	v_readlane_b32 s1, v254, 20
	v_mov_b32_e32 v4, s0
	v_cndmask_b32_e64 v3, v3, v4, s[2:3]
	v_mov_b32_e32 v4, s48
	v_cndmask_b32_e64 v3, v3, v4, s[70:71]
	v_mov_b32_e32 v4, s80
	v_cndmask_b32_e64 v3, v3, v4, s[74:75]
	v_mov_b32_e32 v4, s64
	v_cndmask_b32_e64 v3, v3, v4, s[18:19]
	v_mov_b32_e32 v4, s62
	v_cndmask_b32_e64 v3, v3, v4, s[88:89]
	v_mov_b32_e32 v4, s60
	v_cndmask_b32_e64 v3, v3, v4, s[86:87]
	v_mov_b32_e32 v4, s58
	v_cndmask_b32_e64 v3, v3, v4, s[84:85]
	v_mov_b32_e32 v4, s56
	v_readlane_b32 s0, v254, 21
	v_cndmask_b32_e64 v3, v3, v4, s[72:73]
	v_mov_b32_e32 v4, s42
	v_readlane_b32 s1, v254, 22
	v_cndmask_b32_e64 v3, v3, v4, s[68:69]
	v_mov_b32_e32 v4, s0
	v_readlane_b32 s0, v254, 25
	v_readlane_b32 s1, v254, 26
	v_cndmask_b32_e64 v3, v3, v4, s[92:93]
	v_mov_b32_e32 v4, s0
	v_readlane_b32 s0, v254, 23
	v_readlane_b32 s1, v254, 24
	v_cndmask_b32_e64 v3, v3, v4, s[94:95]
	v_mov_b32_e32 v4, s0
	v_readlane_b32 s0, v254, 27
	v_readlane_b32 s1, v254, 28
	v_readlane_b32 s18, v253, 55
	v_readlane_b32 s2, v253, 51
	v_cndmask_b32_e64 v3, v3, v4, s[66:67]
	v_mov_b32_e32 v4, s0
	v_readlane_b32 s19, v253, 56
	v_readlane_b32 s3, v253, 52
	v_readlane_b32 s0, v253, 53
	s_mov_b32 s3, s19
	v_readlane_b32 s1, v253, 54
	s_lshl_b64 s[0:1], s[0:1], 19
	s_lshl_b64 s[2:3], s[2:3], 8
	v_readlane_b32 s4, v252, 25
	s_add_u32 s4, s4, s0
	v_readlane_b32 s0, v252, 26
	v_cndmask_b32_e64 v3, v3, v4, s[82:83]
	v_mov_b32_e32 v4, s46
	s_addc_u32 s1, s0, s1
	v_cndmask_b32_e32 v3, v3, v4, vcc
	v_mov_b32_e32 v4, s54
	v_writelane_b32 v254, s4, 19
	s_add_u32 s0, s4, s2
	v_cndmask_b32_e64 v3, v3, v4, s[76:77]
	v_writelane_b32 v254, s1, 27
	s_addc_u32 s1, s1, s3
	s_xor_b32 s6, s81, 0x7f
	global_store_dword v122, v3, s[0:1]
	global_store_dword v122, v2, s[0:1] offset:256
	s_lshl_b32 s0, s6, 4
	v_readlane_b32 s1, v253, 39
	s_add_i32 s0, s0, s49
	s_mov_b32 m0, s1
	v_readlane_b32 s1, v253, 41
	v_or_b32_e32 v146, s0, v101
	global_load_lds_dwordx4 v[116:117], off
	s_add_i32 m0, s1, 0x22400
	s_mov_b32 s2, s0
	v_or_b32_e32 v4, s0, v124
	v_readlane_b32 s0, v253, 43
	v_writelane_b32 v254, s2, 23
	v_readlane_b32 s1, v253, 44
	global_load_lds_dwordx4 v[118:119], off
	v_writelane_b32 v254, s3, 24
	v_mov_b64_e32 v[2:3], s[0:1]
	s_movk_i32 s2, 0x2200
	v_mad_u64_u32 v[4:5], s[0:1], v4, s2, v[2:3]
	v_lshl_add_u64 v[4:5], v[4:5], 0, v[106:107]
	v_lshl_add_u64 v[4:5], v[4:5], 0, v[110:111]
	s_mov_b64 s[0:1], 0x1800
	v_lshl_add_u64 v[6:7], v[4:5], 0, s[0:1]
	s_movk_i32 s0, 0x1000
	v_add_co_u32_e32 v4, vcc, s0, v4
	v_mad_u64_u32 v[2:3], s[0:1], v146, s2, v[2:3]
	s_nop 0
	v_addc_co_u32_e32 v5, vcc, 0, v5, vcc
	s_mov_b64 s[0:1], 0x2080
	global_load_dwordx4 v[18:21], v[4:5], off offset:2048
	global_load_dwordx4 v[22:25], v[6:7], off offset:32
	global_load_dwordx4 v[26:29], v[6:7], off offset:64
	global_load_dwordx4 v[30:33], v[6:7], off offset:96
	v_lshl_add_u64 v[4:5], v[2:3], 0, s[0:1]
	v_add_co_u32_e32 v2, vcc, 0x2000, v2
	v_readlane_b32 s83, v253, 45
	s_nop 0
	v_addc_co_u32_e32 v3, vcc, 0, v3, vcc
	global_load_dwordx4 v[6:9], v[2:3], off offset:128
	s_nop 0
	global_load_dwordx4 v[2:5], v[4:5], off offset:16
	s_cmp_gt_i32 s83, 0xdfff
	s_cbranch_scc1 .LBB0_399
	v_readlane_b32 s84, v250, 32
	s_cmp_gt_i32 s83, 0xdfff
	s_mov_b64 s[0:1], -1
	v_readlane_b32 s86, v250, 34
	v_readlane_b32 s87, v250, 35
	v_readlane_b32 s88, v250, 36
	v_readlane_b32 s89, v250, 37
	v_readlane_b32 s90, v250, 38
	v_readlane_b32 s91, v250, 39
	s_movk_i32 s14, 0x100
	v_readlane_b32 s16, v250, 53
	s_mov_b64 s[12:13], 0x88000
	v_readlane_b32 s92, v253, 35
	v_readlane_b32 s85, v250, 33
	v_readlane_b32 s17, v250, 54
	v_readlane_b32 s93, v253, 36
	s_cbranch_scc0 .LBB0_397
	s_add_i32 s0, s83, 0x2000
	s_bfe_u32 s1, s0, 0x70009
	s_mulk_i32 s1, 0x2493
	s_lshr_b32 s3, s1, 16
	s_mul_i32 s1, s3, 0xe00
	s_sub_i32 s0, s0, s1
	s_and_b32 s4, s0, 0xffff
	s_mul_i32 s0, s3, 0x3800000
	s_add_u32 s0, s90, s0
	s_addc_u32 s1, s91, 0
	s_lshl_b32 s2, s4, 1
	s_and_b32 s2, s2, 0x1f80
	v_or_b32_e32 v10, s2, v98
	v_lshlrev_b32_e32 v96, 13, v10
	v_lshl_add_u64 v[10:11], s[0:1], 0, v[96:97]
	s_lshl_b32 s0, s4, 5
	s_and_b32 s0, s0, 0x7e0
	s_lshl_b32 s1, s3, 11
	s_lshl_b32 s18, s0, 2
	s_or_b32 s0, s1, s0
	v_or_b32_e32 v14, s0, v100
	v_readlane_b32 s0, v251, 22
	v_readlane_b32 s1, v251, 23
	s_mov_b32 s3, s19
	v_lshl_add_u64 v[10:11], v[10:11], 0, s[18:19]
	v_mov_b64_e32 v[12:13], s[0:1]
	s_movk_i32 s0, 0x1c00
	v_mad_u64_u32 v[12:13], s[0:1], v14, s0, v[12:13]
	v_lshl_add_u64 v[90:91], v[12:13], 0, s[2:3]
	s_mov_b64 s[0:1], 0

.LBB0_418:
	s_cmp_lt_i32 s83, 0xe000
	s_cselect_b64 s[4:5], -1, 0
	s_and_b64 vcc, exec, s[4:5]
	s_cbranch_vccz .LBB0_423
	s_cmp_gt_i32 s83, 0xdfff
	s_mov_b64 s[0:1], -1
	s_cbranch_scc0 .LBB0_421
	s_add_i32 s0, s83, 0x2000
	s_bfe_u32 s1, s0, 0x70009
	s_mulk_i32 s1, 0x2493
	s_lshr_b32 s3, s1, 16
	s_mul_i32 s1, s3, 0xe00
	s_sub_i32 s0, s0, s1
	s_and_b32 s7, s0, 0xffff
	s_mul_i32 s0, s3, 0x3800000
	s_add_u32 s0, s90, s0
	s_addc_u32 s1, s91, 0
	s_lshl_b32 s8, s7, 1
	s_and_b32 s8, s8, 0x1f80
	v_or_b32_e32 v2, s8, v98
	v_lshlrev_b32_e32 v96, 13, v2
	v_lshl_add_u64 v[2:3], s[0:1], 0, v[96:97]
	s_lshl_b32 s0, s7, 5
	s_and_b32 s0, s0, 0x7e0
	s_lshl_b32 s1, s3, 11
	s_lshl_b32 s18, s0, 2
	s_or_b32 s0, s1, s0
	v_or_b32_e32 v6, s0, v100
	v_readlane_b32 s0, v251, 22
	v_readlane_b32 s1, v251, 23
	s_mov_b32 s9, s19
	v_lshl_add_u64 v[2:3], v[2:3], 0, s[18:19]
	v_mov_b64_e32 v[4:5], s[0:1]
	s_movk_i32 s0, 0x1c00
	v_mad_u64_u32 v[4:5], s[0:1], v6, s0, v[4:5]
	v_lshl_add_u64 v[66:67], v[4:5], 0, s[8:9]
	s_mov_b64 s[0:1], 0

.LBB0_517:
	s_or_b64 exec, exec, s[6:7]
	s_and_saveexec_b64 s[4:5], s[0:1]
	v_mov_b32_e32 v2, s49
	ds_write_b32 v2, v205
	s_or_b64 exec, exec, s[4:5]
	s_add_i32 s59, s59, s40
	s_ashr_i32 s4, s59, 31
	s_add_u32 s5, s59, s39
	s_addc_u32 s4, s4, 0
	v_mov_b32_e32 v69, s4
	v_or_b32_e32 v68, s5, v118
	s_lshl_b32 s4, s58, 9
	v_lshlrev_b64 v[4:5], 12, v[68:69]
	s_or_b32 s30, s4, s41
	v_lshl_add_u64 v[4:5], s[10:11], 0, v[4:5]
	s_lshl_b32 s16, s30, 1
	v_lshl_add_u64 v[4:5], v[4:5], 0, s[16:17]
	v_lshlrev_b32_e32 v2, 1, v122
	v_lshl_add_u64 v[4:5], v[4:5], 0, v[2:3]
	global_load_dwordx4 v[86:89], v[4:5], off
	global_load_dwordx4 v[90:93], v[4:5], off offset:32
	global_load_dwordx4 v[94:97], v[4:5], off offset:64
	global_load_dwordx4 v[98:101], v[4:5], off offset:96
	global_load_dwordx4 v[102:105], v[4:5], off offset:128
	global_load_dwordx4 v[106:109], v[4:5], off offset:160
	global_load_dwordx4 v[110:113], v[4:5], off offset:192
	global_load_dwordx4 v[114:117], v[4:5], off offset:224
	s_cmp_lt_i32 s75, 0xe000
	s_cselect_b64 s[6:7], -1, 0
	s_cmp_gt_i32 s75, 0xdfff
	s_cbranch_scc1 .LBB0_524
	s_cmp_gt_i32 s75, 0xdfff
	s_mov_b64 s[4:5], -1
	s_cbranch_scc0 .LBB0_522
	s_add_i32 s4, s75, 0x2000
	s_bfe_u32 s5, s4, 0x70009
	s_mulk_i32 s5, 0x2493
	s_lshr_b32 s31, s5, 16
	s_mul_i32 s5, s31, 0xe00
	s_sub_i32 s4, s4, s5
	v_readlane_b32 s64, v250, 32
	s_and_b32 s16, s4, 0xffff
	s_mul_i32 s4, s31, 0x3800000
	v_readlane_b32 s70, v250, 38
	v_readlane_b32 s71, v250, 39
	s_add_u32 s4, s70, s4
	s_addc_u32 s5, s71, 0
	s_lshl_b32 s34, s16, 1
	s_and_b32 s34, s34, 0x1f80
	v_or_b32_e32 v2, s34, v124
	v_lshlrev_b32_e32 v2, 13, v2
	v_lshl_add_u64 v[4:5], s[4:5], 0, v[2:3]
	s_lshl_b32 s4, s16, 5
	s_and_b32 s4, s4, 0x7e0
	s_lshl_b32 s5, s31, 11
	s_lshl_b32 s16, s4, 2
	s_or_b32 s4, s5, s4
	v_readlane_b32 s68, v250, 36
	v_readlane_b32 s69, v250, 37
	v_or_b32_e32 v2, s4, v182
	v_mov_b64_e32 v[6:7], s[18:19]
	s_movk_i32 s4, 0x1c00
	v_readlane_b32 s68, v251, 13
	v_mad_u64_u32 v[6:7], s[4:5], v2, s4, v[6:7]
	s_mov_b32 s35, s17
	v_readlane_b32 s65, v250, 33
	v_readlane_b32 s66, v250, 34
	v_readlane_b32 s67, v250, 35
	v_readlane_b32 s69, v251, 14
	v_lshl_add_u64 v[4:5], v[4:5], 0, s[16:17]
	v_lshl_add_u64 v[70:71], v[6:7], 0, s[34:35]
	s_mov_b64 s[4:5], 0

.LBB0_688:
	global_load_dwordx4 v[94:97], v[102:103], off offset:-4096
	global_load_dwordx4 v[90:93], v[102:103], off offset:-3072
	global_load_dwordx4 v[86:89], v[102:103], off offset:-2048
	global_load_dwordx4 v[82:85], v[102:103], off offset:-1024
	global_load_dwordx4 v[78:81], v[102:103], off
	global_load_dwordx4 v[74:77], v[102:103], off offset:1024
	global_load_dwordx4 v[70:73], v[102:103], off offset:2048
	global_load_dwordx4 v[66:69], v[102:103], off offset:3072
	s_cmp_lt_i32 s75, 0xe000
	s_cselect_b64 s[22:23], -1, 0
	s_cmp_gt_i32 s75, 0xdfff
	s_cbranch_scc1 .LBB0_693
	s_cmp_gt_i32 s75, 0xdfff
	s_mov_b64 s[2:3], -1
	s_cbranch_scc0 .LBB0_691
	s_add_i32 s2, s75, 0x2000
	s_bfe_u32 s3, s2, 0x70009
	s_mulk_i32 s3, 0x2493
	s_lshr_b32 s21, s3, 16
	s_mul_i32 s3, s21, 0xe00
	s_sub_i32 s2, s2, s3
	v_readlane_b32 s36, v250, 32
	s_and_b32 s8, s2, 0xffff
	s_mul_i32 s2, s21, 0x3800000
	v_readlane_b32 s42, v250, 38
	v_readlane_b32 s43, v250, 39
	s_add_u32 s2, s42, s2
	s_addc_u32 s3, s43, 0
	s_lshl_b32 s20, s8, 1
	s_and_b32 s20, s20, 0x1f80
	v_or_b32_e32 v2, s20, v98
	v_lshlrev_b32_e32 v100, 13, v2
	v_lshl_add_u64 v[2:3], s[2:3], 0, v[100:101]
	s_lshl_b32 s2, s8, 5
	s_and_b32 s2, s2, 0x7e0
	s_lshl_b32 s3, s21, 11
	s_lshl_b32 s8, s2, 2
	s_or_b32 s2, s3, s2
	v_or_b32_e32 v6, s2, v182
	v_mov_b64_e32 v[4:5], s[10:11]
	v_mad_u64_u32 v[4:5], s[2:3], v6, s7, v[4:5]
	s_mov_b32 s21, s9
	v_readlane_b32 s37, v250, 33
	v_readlane_b32 s38, v250, 34
	v_readlane_b32 s39, v250, 35
	v_readlane_b32 s40, v250, 36
	v_readlane_b32 s41, v250, 37
	v_lshl_add_u64 v[2:3], v[2:3], 0, s[8:9]
	v_lshl_add_u64 v[106:107], v[4:5], 0, s[20:21]
	s_mov_b64 s[2:3], 0

.LBB0_771:
	v_readlane_b32 s0, v250, 44
	v_readlane_b32 s1, v250, 45
	s_andn2_b64 vcc, exec, s[0:1]
	s_cbranch_vccnz .LBB0_805
	s_abs_i32 s0, s97
	v_cvt_f32_u32_e32 v1, s0
	s_sub_i32 s5, 0, s0
	s_add_i32 s1, s97, 0x57f
	s_xor_b32 s4, s1, s97
	v_rcp_iflag_f32_e32 v1, v1
	s_abs_i32 s1, s1
	s_ashr_i32 s4, s4, 31
	v_mul_f32_e32 v1, 0x4f7ffffe, v1
	v_cvt_u32_f32_e32 v1, v1
	s_nop 0
	v_readfirstlane_b32 s6, v1
	s_mul_i32 s5, s5, s6
	s_mul_hi_u32 s5, s6, s5
	s_add_i32 s6, s6, s5
	s_mul_hi_u32 s5, s1, s6
	s_mul_i32 s6, s5, s0
	s_sub_i32 s1, s1, s6
	s_add_i32 s7, s5, 1
	s_sub_i32 s6, s1, s0
	s_cmp_ge_u32 s1, s0
	s_cselect_b32 s5, s7, s5
	s_cselect_b32 s1, s6, s1
	s_add_i32 s6, s5, 1
	s_cmp_ge_u32 s1, s0
	s_cselect_b32 s0, s6, s5
	s_not_b32 s1, s4
	s_xor_b32 s0, s0, s4
	s_add_i32 s0, s1, s0
	s_mul_i32 s0, s0, s97
	s_sub_i32 s4, 0x580, s0
	s_cmp_ge_i32 s4, s97
	s_cselect_b64 s[0:1], -1, 0
	s_cmp_lt_i32 s74, s4
	s_cselect_b64 s[4:5], -1, 0
	s_or_b64 s[0:1], s[0:1], s[4:5]
	s_and_b64 vcc, exec, s[0:1]
	s_cbranch_vccnz .LBB0_805
	s_cmp_gt_i32 s75, 0xdfff
	s_cbranch_scc1 .LBB0_805
	v_readlane_b32 s0, v250, 55
	s_waitcnt vmcnt(16)
	v_and_b32_e32 v2, 7, v0
	v_lshrrev_b32_e32 v3, 3, v178
	s_xor_b32 s14, s0, 0x80000000
	s_cmp_gt_i32 s75, 0xdfff
	v_lshlrev_b32_e32 v1, 4, v3
	v_lshlrev_b32_e32 v134, 2, v2
	v_lshlrev_b32_e32 v2, 4, v2
	s_cbranch_scc0 .LBB0_776
	s_add_i32 s0, s75, 0x2000
	s_bfe_u32 s1, s0, 0x70009
	s_mulk_i32 s1, 0x2493
	s_lshr_b32 s7, s1, 16
	s_mul_i32 s1, s7, 0xe00
	s_sub_i32 s0, s0, s1
	v_readlane_b32 s16, v250, 32
	s_and_b32 s0, s0, 0xffff
	s_mul_i32 s4, s7, 0x3800000
	v_readlane_b32 s22, v250, 38
	v_readlane_b32 s23, v250, 39
	s_add_u32 s4, s22, s4
	s_addc_u32 s5, s23, 0
	s_lshl_b32 s6, s0, 1
	s_and_b32 s6, s6, 0x1f80
	v_lshlrev_b32_e32 v136, 4, v3
	v_or_b32_e32 v3, s6, v136
	v_lshlrev_b32_e32 v4, 13, v3
	v_mov_b32_e32 v5, 0
	s_lshl_b32 s0, s0, 5
	s_waitcnt vmcnt(15)
	v_lshl_add_u64 v[6:7], s[4:5], 0, v[4:5]
	s_and_b32 s4, s0, 0x7e0
	s_mov_b32 s1, 0
	s_lshl_b32 s0, s4, 2
	v_lshl_add_u64 v[6:7], v[6:7], 0, s[0:1]
	s_lshl_b32 s0, s7, 11
	v_mov_b32_e32 v3, v5
	s_or_b32 s0, s0, s4
	v_mov_b32_e32 v135, v5
	v_lshl_add_u64 v[6:7], v[6:7], 0, v[2:3]
	v_or_b32_e32 v3, s0, v134
	s_movk_i32 s0, 0x1c00
	v_mov_b64_e32 v[4:5], s[78:79]
	v_mad_u64_u32 v[4:5], s[4:5], v3, s0, v[4:5]
	s_mov_b32 s7, s1
	v_lshl_add_u64 v[4:5], v[4:5], 0, s[6:7]
	s_mov_b64 s[0:1], 0x24500000
	v_readlane_b32 s17, v250, 33
	v_readlane_b32 s18, v250, 34
	v_readlane_b32 s19, v250, 35
	v_readlane_b32 s20, v250, 36
	v_readlane_b32 s21, v250, 37
	v_lshl_add_u64 v[66:67], v[4:5], 0, s[0:1]
	s_mov_b64 s[0:1], 0
	s_mov_b32 s15, 0x43000000
	s_branch .LBB0_777

.LBB0_1212:
	v_readlane_b32 s0, v250, 44
	v_readlane_b32 s1, v250, 45
	s_andn2_b64 vcc, exec, s[0:1]
	s_cbranch_vccnz .LBB0_1246
	s_abs_i32 s0, s97
	v_cvt_f32_u32_e32 v1, s0
	s_sub_i32 s7, 0, s0
	s_add_i32 s1, s97, 0x47f
	s_xor_b32 s6, s1, s97
	v_rcp_iflag_f32_e32 v1, v1
	s_abs_i32 s1, s1
	s_ashr_i32 s6, s6, 31
	v_mul_f32_e32 v1, 0x4f7ffffe, v1
	v_cvt_u32_f32_e32 v1, v1
	s_nop 0
	v_readfirstlane_b32 s8, v1
	s_mul_i32 s7, s7, s8
	s_mul_hi_u32 s7, s8, s7
	s_add_i32 s8, s8, s7
	s_mul_hi_u32 s7, s1, s8
	s_mul_i32 s8, s7, s0
	s_sub_i32 s1, s1, s8
	s_add_i32 s9, s7, 1
	s_sub_i32 s8, s1, s0
	s_cmp_ge_u32 s1, s0
	s_cselect_b32 s7, s9, s7
	s_cselect_b32 s1, s8, s1
	s_add_i32 s8, s7, 1
	s_cmp_ge_u32 s1, s0
	s_cselect_b32 s0, s8, s7
	s_not_b32 s1, s6
	s_xor_b32 s0, s0, s6
	s_add_i32 s0, s1, s0
	s_mul_i32 s0, s0, s97
	s_sub_i32 s6, 0x480, s0
	s_cmp_ge_i32 s6, s97
	s_cselect_b64 s[0:1], -1, 0
	s_cmp_lt_i32 s74, s6
	s_cselect_b64 s[6:7], -1, 0
	s_or_b64 s[0:1], s[0:1], s[6:7]
	s_and_b64 vcc, exec, s[0:1]
	s_cbranch_vccnz .LBB0_1246
	s_cmp_gt_i32 s75, 0xdfff
	s_cbranch_scc1 .LBB0_1246
	v_readlane_b32 s0, v250, 55
	s_waitcnt vmcnt(0)
	v_and_b32_e32 v2, 7, v0
	v_lshrrev_b32_e32 v3, 3, v178
	s_xor_b32 s16, s0, 0x80000000
	s_cmp_gt_i32 s75, 0xdfff
	v_lshlrev_b32_e32 v1, 4, v3
	v_lshlrev_b32_e32 v134, 2, v2
	v_lshlrev_b32_e32 v2, 4, v2
	s_cbranch_scc0 .LBB0_1217
	s_add_i32 s0, s75, 0x2000
	s_bfe_u32 s1, s0, 0x70009
	s_mulk_i32 s1, 0x2493
	s_lshr_b32 s9, s1, 16
	s_mul_i32 s1, s9, 0xe00
	s_sub_i32 s0, s0, s1
	v_readlane_b32 s24, v250, 32
	s_and_b32 s0, s0, 0xffff
	s_mul_i32 s6, s9, 0x3800000
	v_readlane_b32 s30, v250, 38
	v_readlane_b32 s31, v250, 39
	s_add_u32 s6, s30, s6
	s_addc_u32 s7, s31, 0
	s_lshl_b32 s8, s0, 1
	s_and_b32 s8, s8, 0x1f80
	v_lshlrev_b32_e32 v136, 4, v3
	v_or_b32_e32 v3, s8, v136
	v_lshlrev_b32_e32 v4, 13, v3
	v_mov_b32_e32 v5, 0
	s_lshl_b32 s0, s0, 5
	v_lshl_add_u64 v[6:7], s[6:7], 0, v[4:5]
	s_and_b32 s6, s0, 0x7e0
	s_mov_b32 s1, 0
	s_lshl_b32 s0, s6, 2
	v_lshl_add_u64 v[6:7], v[6:7], 0, s[0:1]
	s_lshl_b32 s0, s9, 11
	v_mov_b32_e32 v3, v5
	s_or_b32 s0, s0, s6
	v_mov_b32_e32 v135, v5
	v_lshl_add_u64 v[6:7], v[6:7], 0, v[2:3]
	v_or_b32_e32 v3, s0, v134
	s_movk_i32 s0, 0x1c00
	v_mov_b64_e32 v[4:5], s[78:79]
	v_mad_u64_u32 v[4:5], s[6:7], v3, s0, v[4:5]
	s_mov_b32 s9, s1
	v_lshl_add_u64 v[4:5], v[4:5], 0, s[8:9]
	s_mov_b64 s[0:1], 0x24500000
	v_readlane_b32 s25, v250, 33
	v_readlane_b32 s26, v250, 34
	v_readlane_b32 s27, v250, 35
	v_readlane_b32 s28, v250, 36
	v_readlane_b32 s29, v250, 37
	v_lshl_add_u64 v[66:67], v[4:5], 0, s[0:1]
	s_mov_b64 s[0:1], 0
	s_mov_b32 s17, 0x43000000
	s_branch .LBB0_1218

.LBB0_1223:
	s_cmp_gt_i32 s19, 0
	s_cselect_b64 s[0:1], -1, 0
	s_cmp_lt_i32 s75, 0xe000
	s_cselect_b64 s[14:15], -1, 0
	s_and_b64 s[14:15], s[0:1], s[14:15]
	v_cndmask_b32_e64 v130, 0, 1, s[14:15]
	v_cmp_ne_u32_e64 s[0:1], 1, v130
	s_andn2_b64 vcc, exec, s[14:15]
	s_cbranch_vccnz .LBB0_1230
	s_cmp_gt_i32 s75, 0xdfff
	s_mov_b64 s[12:13], -1
	s_cbranch_scc0 .LBB0_1226
	s_add_i32 s12, s75, 0x2000
	s_bfe_u32 s13, s12, 0x70009
	s_mulk_i32 s13, 0x2493
	s_lshr_b32 s15, s13, 16
	s_mul_i32 s13, s15, 0xe00
	s_sub_i32 s12, s12, s13
	v_readlane_b32 s36, v250, 32
	s_and_b32 s25, s12, 0xffff
	s_mul_i32 s12, s15, 0x3800000
	v_readlane_b32 s42, v250, 38
	v_readlane_b32 s43, v250, 39
	s_add_u32 s12, s42, s12
	s_addc_u32 s13, s43, 0
	s_lshl_b32 s14, s25, 1
	s_and_b32 s14, s14, 0x1f80
	s_waitcnt vmcnt(16)
	v_or_b32_e32 v66, s14, v136
	v_lshlrev_b32_e32 v138, 13, v66
	v_lshl_add_u64 v[66:67], s[12:13], 0, v[138:139]
	s_lshl_b32 s12, s25, 5
	s_and_b32 s25, s12, 0x7e0
	s_lshl_b32 s12, s25, 2
	s_mov_b32 s13, s7
	v_lshl_add_u64 v[66:67], v[66:67], 0, s[12:13]
	s_lshl_b32 s12, s15, 11
	s_or_b32 s12, s12, s25
	v_or_b32_e32 v68, s12, v134
	v_mul_hi_i32_i24_e32 v69, 0x1c00, v68
	v_mul_i32_i24_e32 v68, 0x1c00, v68
	v_lshl_add_u64 v[68:69], s[8:9], 0, v[68:69]
	s_mov_b32 s15, s7
	v_readlane_b32 s37, v250, 33
	v_readlane_b32 s38, v250, 34
	v_readlane_b32 s39, v250, 35
	v_readlane_b32 s40, v250, 36
	v_readlane_b32 s41, v250, 37
	v_lshl_add_u64 v[130:131], v[68:69], 0, s[14:15]
	s_mov_b64 s[12:13], 0

.LBB0_1234:
	v_mad_u64_u32 v[144:145], s[14:15], s6, 3, v[140:141]
	s_and_b64 vcc, exec, s[0:1]
	s_mov_b64 s[0:1], 0
	global_store_dwordx4 v[144:145], v[130:133], off
	s_cbranch_vccnz .LBB0_1222
	s_cmp_gt_i32 s19, 0
	s_cselect_b64 s[0:1], -1, 0
	s_cmp_lt_i32 s75, 0xe000
	s_cselect_b64 s[14:15], -1, 0
	s_and_b64 s[0:1], s[0:1], s[14:15]
	s_andn2_b64 vcc, exec, s[0:1]
	s_cbranch_vccnz .LBB0_1242
	s_cmp_gt_i32 s75, 0xdfff
	s_mov_b64 s[14:15], -1
	s_cbranch_scc0 .LBB0_1238
	s_add_i32 s6, s75, 0x2000
	s_bfe_u32 s13, s6, 0x70009
	s_mulk_i32 s13, 0x2493
	s_lshr_b32 s13, s13, 16
	s_mul_i32 s14, s13, 0xe00
	s_sub_i32 s6, s6, s14
	v_readlane_b32 s36, v250, 32
	s_and_b32 s6, s6, 0xffff
	s_mul_i32 s14, s13, 0x3800000
	v_readlane_b32 s42, v250, 38
	v_readlane_b32 s43, v250, 39
	s_add_u32 s14, s42, s14
	s_addc_u32 s15, s43, 0
	s_lshl_b32 s17, s6, 1
	s_and_b32 s26, s17, 0x1f80
	s_waitcnt vmcnt(16)
	v_or_b32_e32 v2, s26, v136
	v_lshlrev_b32_e32 v138, 13, v2
	s_lshl_b32 s6, s6, 5
	v_lshl_add_u64 v[2:3], s[14:15], 0, v[138:139]
	s_and_b32 s14, s6, 0x7e0
	s_lshl_b32 s6, s14, 2
	v_lshl_add_u64 v[2:3], v[2:3], 0, s[6:7]
	s_lshl_b32 s6, s13, 11
	s_or_b32 s6, s6, s14
	v_or_b32_e32 v4, s6, v134
	v_mul_hi_i32_i24_e32 v5, 0x1c00, v4
	v_mul_i32_i24_e32 v4, 0x1c00, v4
	v_lshl_add_u64 v[4:5], s[8:9], 0, v[4:5]
	s_mov_b32 s27, s7
	v_readlane_b32 s37, v250, 33
	v_readlane_b32 s38, v250, 34
	v_readlane_b32 s39, v250, 35
	v_readlane_b32 s40, v250, 36
	v_readlane_b32 s41, v250, 37
	v_lshl_add_u64 v[130:131], v[4:5], 0, s[26:27]
	s_mov_b64 s[14:15], 0

.LBB0_1603:
	s_or_b64 exec, exec, s[2:3]
	s_abs_i32 s29, s28
	v_cvt_f32_u32_e32 v1, s29
	s_add_i32 s2, s28, 0xdfff
	s_sub_i32 s5, 0, s29
	s_xor_b32 s3, s2, s28
	v_rcp_iflag_f32_e32 v1, v1
	s_ashr_i32 s4, s3, 31
	s_abs_i32 s2, s2
	s_mov_b32 s25, 0
	v_mul_f32_e32 v1, 0x4f7ffffe, v1
	v_cvt_u32_f32_e32 v1, v1
	s_waitcnt lgkmcnt(0)
	s_barrier
	v_readfirstlane_b32 s30, v1
	s_mul_i32 s5, s5, s30
	s_mul_hi_u32 s3, s30, s5
	s_add_i32 s30, s30, s3
	s_mul_hi_u32 s3, s2, s30
	s_mul_i32 s5, s3, s29
	s_sub_i32 s2, s2, s5
	s_add_i32 s6, s3, 1
	s_sub_i32 s5, s2, s29
	s_cmp_ge_u32 s2, s29
	s_cselect_b32 s3, s6, s3
	s_cselect_b32 s2, s5, s2
	s_add_i32 s5, s3, 1
	s_cmp_ge_u32 s2, s29
	s_cselect_b32 s2, s5, s3
	s_xor_b32 s5, s2, s4
	v_readlane_b32 s2, v250, 53
	s_cmpk_lt_i32 s2, 0x2000
	v_readlane_b32 s3, v250, 54
	s_cbranch_scc1 .LBB0_1605
	v_mov_b32_e32 v183, 0
	v_readlane_b32 s2, v250, 55
	v_and_b32_e32 v98, 0x70, v198
	s_xor_b32 s33, s2, 0x80000000
	v_mov_b32_e32 v99, v183
	s_sub_i32 s31, s5, s4
	s_cbranch_execz .LBB0_1606
	s_branch .LBB0_1635

.LBB0_1610:
	s_abs_i32 s3, s8
	s_mul_hi_u32 s4, s3, s30
	s_mul_i32 s4, s4, s29
	s_sub_i32 s3, s3, s4
	s_ashr_i32 s2, s8, 31
	s_sub_i32 s4, s3, s29
	s_cmp_ge_u32 s3, s29
	s_cselect_b32 s3, s4, s3
	s_sub_i32 s4, s3, s29
	s_cmp_ge_u32 s3, s29
	s_cselect_b32 s3, s4, s3
	s_xor_b32 s3, s3, s2
	s_sub_i32 s4, s3, s2
	s_add_i32 s48, s7, s4
	s_cmp_gt_i32 s48, 0xdfff
	s_cselect_b64 s[2:3], -1, 0
	s_and_b64 vcc, exec, s[2:3]
	s_cbranch_vccnz .LBB0_1612
	s_lshl_b32 s2, s4, 2
	s_add_i32 s2, s2, 0
	s_add_i32 s2, s2, 0x20400
	v_mov_b32_e32 v100, s2
	ds_read_b32 v100, v100
	s_waitcnt lgkmcnt(0)
	v_cmp_lt_i32_e64 s[2:3], s48, v100

.LBB0_1641:
	s_abs_i32 s7, s17
	s_mul_hi_u32 s8, s7, s30
	s_mul_i32 s8, s8, s29
	s_sub_i32 s7, s7, s8
	s_ashr_i32 s6, s17, 31
	s_sub_i32 s8, s7, s29
	s_cmp_ge_u32 s7, s29
	s_cselect_b32 s7, s8, s7
	s_sub_i32 s8, s7, s29
	s_cmp_ge_u32 s7, s29
	s_cselect_b32 s7, s8, s7
	s_xor_b32 s7, s7, s6
	s_sub_i32 s6, s7, s6
	s_add_i32 s16, s4, s6
	s_cmp_gt_i32 s16, 0xdfff
	s_cselect_b64 s[8:9], -1, 0
	s_and_b64 vcc, exec, s[8:9]
	s_cbranch_vccnz .LBB0_1643
	s_lshl_b32 s6, s6, 2
	s_add_i32 s6, s6, 0
	s_add_i32 s6, s6, 0x20400
	v_mov_b32_e32 v2, s6
	ds_read_b32 v2, v2
	s_waitcnt lgkmcnt(0)
	v_cmp_lt_i32_e64 s[8:9], s16, v2

.LBB0_1707:
	v_readlane_b32 s4, v250, 40
	s_cmp_lt_i32 s4, 18
	v_readlane_b32 s5, v250, 41
	s_cselect_b64 s[0:1], -1, 0
	s_cmp_gt_i32 s4, 17
	s_cselect_b64 s[2:3], -1, 0
	s_cmp_lt_i32 s5, 18
	s_cselect_b64 s[4:5], -1, 0
	s_or_b64 s[2:3], s[2:3], s[4:5]
	s_and_b64 vcc, exec, s[2:3]
	s_cbranch_vccnz .LBB0_1731
	v_readfirstlane_b32 s8, v0
	s_lshr_b32 s8, s8, 6
	s_cmp_eq_u32 s97, 0x100
	s_cbranch_scc0 .Lcv17_all
	s_cmpk_lt_i32 s74, 0xe0
	s_cbranch_scc1 .Lcv17_gemm
	s_sub_u32 s6, s74, 0xe0
	s_lshl_b32 s6, s6, 3
	s_add_u32 s6, s6, s8
	s_movk_i32 s7, 0x100
	s_mov_b32 s17, 0
	s_branch .Lcv17_conv
.Lcv17_all:
	s_lshl_b32 s6, s74, 3
	s_add_u32 s6, s6, s8
	s_lshl_b32 s7, s97, 3
	s_mov_b32 s17, 1
.Lcv17_conv:
	v_and_b32_e32 v150, 63, v0
	v_lshrrev_b32_e32 v151, 3, v150
	v_and_b32_e32 v152, 7, v150
	v_lshlrev_b32_e32 v130, 17, v151
	v_lshl_add_u32 v130, v152, 4, v130
	v_add_u32_e32 v131, 0x2000, v130
	v_add_u32_e32 v132, 0x4000, v130
	v_add_u32_e32 v133, 0x6000, v130
	v_add_u32_e32 v134, 0x8000, v130
	v_add_u32_e32 v135, 0xa000, v130
	v_add_u32_e32 v136, 0xc000, v130
	v_add_u32_e32 v137, 0xe000, v130
	v_add_u32_e32 v138, 0x10000, v130
	v_add_u32_e32 v139, 0x12000, v130
	v_add_u32_e32 v140, 0x14000, v130
	v_add_u32_e32 v141, 0x16000, v130
	v_add_u32_e32 v142, 0x18000, v130
	v_add_u32_e32 v143, 0x1a000, v130
	v_add_u32_e32 v144, 0x1c000, v130
	v_add_u32_e32 v145, 0x1e000, v130
	v_lshlrev_b32_e32 v146, 4, v151
	v_mul_u32_u24_e32 v153, 0x7000, v152
	v_add_u32_e32 v146, v146, v153
	v_add_u32_e32 v147, 0x1c00, v146
	v_add_u32_e32 v148, 0x3800, v146
	v_add_u32_e32 v149, 0x5400, v146
	v_readlane_b32 s12, v250, 38
	v_readlane_b32 s13, v250, 39
	s_add_u32 s14, s78, 0x24500000
	s_addc_u32 s15, s79, 0
	s_mov_b32 s16, 0x43000000
	s_cmpk_lt_u32 s6, 0x7000
	s_cbranch_scc0 .Lcv17_done
	s_lshr_b32 s8, s6, 6
	s_and_b32 s9, s6, 63
	s_lshl_b32 s10, s8, 20
	s_lshl_b32 s11, s9, 7
	s_add_u32 s10, s10, s11
	s_add_u32 s2, s12, s10
	s_addc_u32 s3, s13, 0
	s_mul_i32 s10, s8, 0x4925
	s_lshr_b32 s10, s10, 20
	s_mul_i32 s11, s10, 56
	s_sub_u32 s8, s8, s11
	s_mul_i32 s10, s10, 0xe00000
	s_lshl_b32 s8, s8, 7
	s_add_u32 s10, s10, s8
	s_mul_i32 s9, s9, 0x38000
	s_add_u32 s10, s10, s9
	s_add_u32 s4, s14, s10
	s_addc_u32 s5, s15, 0
	global_load_dwordx4 v[2:5], v130, s[2:3]
	global_load_dwordx4 v[6:9], v131, s[2:3]
	global_load_dwordx4 v[10:13], v132, s[2:3]
	global_load_dwordx4 v[14:17], v133, s[2:3]
	global_load_dwordx4 v[18:21], v134, s[2:3]
	global_load_dwordx4 v[22:25], v135, s[2:3]
	global_load_dwordx4 v[26:29], v136, s[2:3]
	global_load_dwordx4 v[30:33], v137, s[2:3]
	global_load_dwordx4 v[34:37], v138, s[2:3]
	global_load_dwordx4 v[38:41], v139, s[2:3]
	global_load_dwordx4 v[42:45], v140, s[2:3]
	global_load_dwordx4 v[46:49], v141, s[2:3]
	global_load_dwordx4 v[50:53], v142, s[2:3]
	global_load_dwordx4 v[54:57], v143, s[2:3]
	global_load_dwordx4 v[58:61], v144, s[2:3]
	global_load_dwordx4 v[62:65], v145, s[2:3]
	s_add_u32 s6, s6, s7
	s_cmpk_lt_u32 s6, 0x7000
	s_cbranch_scc0 .Lcv17_tailA
	s_lshr_b32 s8, s6, 6
	s_and_b32 s9, s6, 63
	s_lshl_b32 s10, s8, 20
	s_lshl_b32 s11, s9, 7
	s_add_u32 s10, s10, s11
	s_add_u32 s2, s12, s10
	s_addc_u32 s3, s13, 0
	s_mul_i32 s10, s8, 0x4925
	s_lshr_b32 s10, s10, 20
	s_mul_i32 s11, s10, 56
	s_sub_u32 s8, s8, s11
	s_mul_i32 s10, s10, 0xe00000
	s_lshl_b32 s8, s8, 7
	s_add_u32 s10, s10, s8
	s_mul_i32 s9, s9, 0x38000
	s_add_u32 s10, s10, s9
	s_add_u32 s18, s14, s10
	s_addc_u32 s19, s15, 0
	global_load_dwordx4 v[66:69], v130, s[2:3]
	global_load_dwordx4 v[70:73], v131, s[2:3]
	global_load_dwordx4 v[74:77], v132, s[2:3]
	global_load_dwordx4 v[78:81], v133, s[2:3]
	global_load_dwordx4 v[82:85], v134, s[2:3]
	global_load_dwordx4 v[86:89], v135, s[2:3]
	global_load_dwordx4 v[90:93], v136, s[2:3]
	global_load_dwordx4 v[94:97], v137, s[2:3]
	global_load_dwordx4 v[98:101], v138, s[2:3]
	global_load_dwordx4 v[102:105], v139, s[2:3]
	global_load_dwordx4 v[106:109], v140, s[2:3]
	global_load_dwordx4 v[110:113], v141, s[2:3]
	global_load_dwordx4 v[114:117], v142, s[2:3]
	global_load_dwordx4 v[118:121], v143, s[2:3]
	global_load_dwordx4 v[122:125], v144, s[2:3]
	global_load_dwordx4 v[126:129], v145, s[2:3]
	s_waitcnt vmcnt(16)
	v_mul_f32_e32 v2, s16, v2
	v_mul_f32_e32 v3, s16, v3
	v_mul_f32_e32 v4, s16, v4
	v_mul_f32_e32 v5, s16, v5
	v_mul_f32_e32 v6, s16, v6
	v_mul_f32_e32 v7, s16, v7
	v_mul_f32_e32 v8, s16, v8
	v_mul_f32_e32 v9, s16, v9
	v_mul_f32_e32 v10, s16, v10
	v_mul_f32_e32 v11, s16, v11
	v_mul_f32_e32 v12, s16, v12
	v_mul_f32_e32 v13, s16, v13
	v_mul_f32_e32 v14, s16, v14
	v_mul_f32_e32 v15, s16, v15
	v_mul_f32_e32 v16, s16, v16
	v_mul_f32_e32 v17, s16, v17
	v_mul_f32_e32 v18, s16, v18
	v_mul_f32_e32 v19, s16, v19
	v_mul_f32_e32 v20, s16, v20
	v_mul_f32_e32 v21, s16, v21
	v_mul_f32_e32 v22, s16, v22
	v_mul_f32_e32 v23, s16, v23
	v_mul_f32_e32 v24, s16, v24
	v_mul_f32_e32 v25, s16, v25
	v_mul_f32_e32 v26, s16, v26
	v_mul_f32_e32 v27, s16, v27
	v_mul_f32_e32 v28, s16, v28
	v_mul_f32_e32 v29, s16, v29
	v_mul_f32_e32 v30, s16, v30
	v_mul_f32_e32 v31, s16, v31
	v_mul_f32_e32 v32, s16, v32
	v_mul_f32_e32 v33, s16, v33
	v_mul_f32_e32 v34, s16, v34
	v_mul_f32_e32 v35, s16, v35
	v_mul_f32_e32 v36, s16, v36
	v_mul_f32_e32 v37, s16, v37
	v_mul_f32_e32 v38, s16, v38
	v_mul_f32_e32 v39, s16, v39
	v_mul_f32_e32 v40, s16, v40
	v_mul_f32_e32 v41, s16, v41
	v_mul_f32_e32 v42, s16, v42
	v_mul_f32_e32 v43, s16, v43
	v_mul_f32_e32 v44, s16, v44
	v_mul_f32_e32 v45, s16, v45
	v_mul_f32_e32 v46, s16, v46
	v_mul_f32_e32 v47, s16, v47
	v_mul_f32_e32 v48, s16, v48
	v_mul_f32_e32 v49, s16, v49
	v_mul_f32_e32 v50, s16, v50
	v_mul_f32_e32 v51, s16, v51
	v_mul_f32_e32 v52, s16, v52
	v_mul_f32_e32 v53, s16, v53
	v_mul_f32_e32 v54, s16, v54
	v_mul_f32_e32 v55, s16, v55
	v_mul_f32_e32 v56, s16, v56
	v_mul_f32_e32 v57, s16, v57
	v_mul_f32_e32 v58, s16, v58
	v_mul_f32_e32 v59, s16, v59
	v_mul_f32_e32 v60, s16, v60
	v_mul_f32_e32 v61, s16, v61
	v_mul_f32_e32 v62, s16, v62
	v_mul_f32_e32 v63, s16, v63
	v_mul_f32_e32 v64, s16, v64
	v_mul_f32_e32 v65, s16, v65
	v_cvt_pk_fp8_f32 v150, v2, v6
	v_cvt_pk_fp8_f32 v151, v18, v22
	v_cvt_pk_fp8_f32 v152, v34, v38
	v_cvt_pk_fp8_f32 v153, v50, v54
	v_cvt_pk_fp8_f32 v154, v3, v7
	v_cvt_pk_fp8_f32 v155, v19, v23
	v_cvt_pk_fp8_f32 v156, v35, v39
	v_cvt_pk_fp8_f32 v157, v51, v55
	v_cvt_pk_fp8_f32 v158, v4, v8
	v_cvt_pk_fp8_f32 v159, v20, v24
	v_cvt_pk_fp8_f32 v160, v36, v40
	v_cvt_pk_fp8_f32 v161, v52, v56
	v_cvt_pk_fp8_f32 v162, v5, v9
	v_cvt_pk_fp8_f32 v163, v21, v25
	v_cvt_pk_fp8_f32 v164, v37, v41
	v_cvt_pk_fp8_f32 v165, v53, v57
	v_cvt_pk_fp8_f32 v150, v10, v14 op_sel:[0,0,1]
	v_cvt_pk_fp8_f32 v151, v26, v30 op_sel:[0,0,1]
	v_cvt_pk_fp8_f32 v152, v42, v46 op_sel:[0,0,1]
	v_cvt_pk_fp8_f32 v153, v58, v62 op_sel:[0,0,1]
	v_cvt_pk_fp8_f32 v154, v11, v15 op_sel:[0,0,1]
	v_cvt_pk_fp8_f32 v155, v27, v31 op_sel:[0,0,1]
	v_cvt_pk_fp8_f32 v156, v43, v47 op_sel:[0,0,1]
	v_cvt_pk_fp8_f32 v157, v59, v63 op_sel:[0,0,1]
	v_cvt_pk_fp8_f32 v158, v12, v16 op_sel:[0,0,1]
	v_cvt_pk_fp8_f32 v159, v28, v32 op_sel:[0,0,1]
	v_cvt_pk_fp8_f32 v160, v44, v48 op_sel:[0,0,1]
	v_cvt_pk_fp8_f32 v161, v60, v64 op_sel:[0,0,1]
	v_cvt_pk_fp8_f32 v162, v13, v17 op_sel:[0,0,1]
	v_cvt_pk_fp8_f32 v163, v29, v33 op_sel:[0,0,1]
	v_cvt_pk_fp8_f32 v164, v45, v49 op_sel:[0,0,1]
	v_cvt_pk_fp8_f32 v165, v61, v65 op_sel:[0,0,1]
	s_nop 1
	global_store_dwordx4 v146, v[150:153], s[4:5]
	global_store_dwordx4 v147, v[154:157], s[4:5]
	global_store_dwordx4 v148, v[158:161], s[4:5]
	global_store_dwordx4 v149, v[162:165], s[4:5]
.Lcv17_loop:
	s_add_u32 s6, s6, s7
	s_cmpk_lt_u32 s6, 0x7000
	s_cbranch_scc0 .Lcv17_tailB
	s_lshr_b32 s8, s6, 6
	s_and_b32 s9, s6, 63
	s_lshl_b32 s10, s8, 20
	s_lshl_b32 s11, s9, 7
	s_add_u32 s10, s10, s11
	s_add_u32 s2, s12, s10
	s_addc_u32 s3, s13, 0
	s_mul_i32 s10, s8, 0x4925
	s_lshr_b32 s10, s10, 20
	s_mul_i32 s11, s10, 56
	s_sub_u32 s8, s8, s11
	s_mul_i32 s10, s10, 0xe00000
	s_lshl_b32 s8, s8, 7
	s_add_u32 s10, s10, s8
	s_mul_i32 s9, s9, 0x38000
	s_add_u32 s10, s10, s9
	s_add_u32 s4, s14, s10
	s_addc_u32 s5, s15, 0
	global_load_dwordx4 v[2:5], v130, s[2:3]
	global_load_dwordx4 v[6:9], v131, s[2:3]
	global_load_dwordx4 v[10:13], v132, s[2:3]
	global_load_dwordx4 v[14:17], v133, s[2:3]
	global_load_dwordx4 v[18:21], v134, s[2:3]
	global_load_dwordx4 v[22:25], v135, s[2:3]
	global_load_dwordx4 v[26:29], v136, s[2:3]
	global_load_dwordx4 v[30:33], v137, s[2:3]
	global_load_dwordx4 v[34:37], v138, s[2:3]
	global_load_dwordx4 v[38:41], v139, s[2:3]
	global_load_dwordx4 v[42:45], v140, s[2:3]
	global_load_dwordx4 v[46:49], v141, s[2:3]
	global_load_dwordx4 v[50:53], v142, s[2:3]
	global_load_dwordx4 v[54:57], v143, s[2:3]
	global_load_dwordx4 v[58:61], v144, s[2:3]
	global_load_dwordx4 v[62:65], v145, s[2:3]
	s_waitcnt vmcnt(20)
	v_mul_f32_e32 v66, s16, v66
	v_mul_f32_e32 v67, s16, v67
	v_mul_f32_e32 v68, s16, v68
	v_mul_f32_e32 v69, s16, v69
	v_mul_f32_e32 v70, s16, v70
	v_mul_f32_e32 v71, s16, v71
	v_mul_f32_e32 v72, s16, v72
	v_mul_f32_e32 v73, s16, v73
	v_mul_f32_e32 v74, s16, v74
	v_mul_f32_e32 v75, s16, v75
	v_mul_f32_e32 v76, s16, v76
	v_mul_f32_e32 v77, s16, v77
	v_mul_f32_e32 v78, s16, v78
	v_mul_f32_e32 v79, s16, v79
	v_mul_f32_e32 v80, s16, v80
	v_mul_f32_e32 v81, s16, v81
	v_mul_f32_e32 v82, s16, v82
	v_mul_f32_e32 v83, s16, v83
	v_mul_f32_e32 v84, s16, v84
	v_mul_f32_e32 v85, s16, v85
	v_mul_f32_e32 v86, s16, v86
	v_mul_f32_e32 v87, s16, v87
	v_mul_f32_e32 v88, s16, v88
	v_mul_f32_e32 v89, s16, v89
	v_mul_f32_e32 v90, s16, v90
	v_mul_f32_e32 v91, s16, v91
	v_mul_f32_e32 v92, s16, v92
	v_mul_f32_e32 v93, s16, v93
	v_mul_f32_e32 v94, s16, v94
	v_mul_f32_e32 v95, s16, v95
	v_mul_f32_e32 v96, s16, v96
	v_mul_f32_e32 v97, s16, v97
	v_mul_f32_e32 v98, s16, v98
	v_mul_f32_e32 v99, s16, v99
	v_mul_f32_e32 v100, s16, v100
	v_mul_f32_e32 v101, s16, v101
	v_mul_f32_e32 v102, s16, v102
	v_mul_f32_e32 v103, s16, v103
	v_mul_f32_e32 v104, s16, v104
	v_mul_f32_e32 v105, s16, v105
	v_mul_f32_e32 v106, s16, v106
	v_mul_f32_e32 v107, s16, v107
	v_mul_f32_e32 v108, s16, v108
	v_mul_f32_e32 v109, s16, v109
	v_mul_f32_e32 v110, s16, v110
	v_mul_f32_e32 v111, s16, v111
	v_mul_f32_e32 v112, s16, v112
	v_mul_f32_e32 v113, s16, v113
	v_mul_f32_e32 v114, s16, v114
	v_mul_f32_e32 v115, s16, v115
	v_mul_f32_e32 v116, s16, v116
	v_mul_f32_e32 v117, s16, v117
	v_mul_f32_e32 v118, s16, v118
	v_mul_f32_e32 v119, s16, v119
	v_mul_f32_e32 v120, s16, v120
	v_mul_f32_e32 v121, s16, v121
	v_mul_f32_e32 v122, s16, v122
	v_mul_f32_e32 v123, s16, v123
	v_mul_f32_e32 v124, s16, v124
	v_mul_f32_e32 v125, s16, v125
	v_mul_f32_e32 v126, s16, v126
	v_mul_f32_e32 v127, s16, v127
	v_mul_f32_e32 v128, s16, v128
	v_mul_f32_e32 v129, s16, v129
	v_cvt_pk_fp8_f32 v150, v66, v70
	v_cvt_pk_fp8_f32 v151, v82, v86
	v_cvt_pk_fp8_f32 v152, v98, v102
	v_cvt_pk_fp8_f32 v153, v114, v118
	v_cvt_pk_fp8_f32 v154, v67, v71
	v_cvt_pk_fp8_f32 v155, v83, v87
	v_cvt_pk_fp8_f32 v156, v99, v103
	v_cvt_pk_fp8_f32 v157, v115, v119
	v_cvt_pk_fp8_f32 v158, v68, v72
	v_cvt_pk_fp8_f32 v159, v84, v88
	v_cvt_pk_fp8_f32 v160, v100, v104
	v_cvt_pk_fp8_f32 v161, v116, v120
	v_cvt_pk_fp8_f32 v162, v69, v73
	v_cvt_pk_fp8_f32 v163, v85, v89
	v_cvt_pk_fp8_f32 v164, v101, v105
	v_cvt_pk_fp8_f32 v165, v117, v121
	v_cvt_pk_fp8_f32 v150, v74, v78 op_sel:[0,0,1]
	v_cvt_pk_fp8_f32 v151, v90, v94 op_sel:[0,0,1]
	v_cvt_pk_fp8_f32 v152, v106, v110 op_sel:[0,0,1]
	v_cvt_pk_fp8_f32 v153, v122, v126 op_sel:[0,0,1]
	v_cvt_pk_fp8_f32 v154, v75, v79 op_sel:[0,0,1]
	v_cvt_pk_fp8_f32 v155, v91, v95 op_sel:[0,0,1]
	v_cvt_pk_fp8_f32 v156, v107, v111 op_sel:[0,0,1]
	v_cvt_pk_fp8_f32 v157, v123, v127 op_sel:[0,0,1]
	v_cvt_pk_fp8_f32 v158, v76, v80 op_sel:[0,0,1]
	v_cvt_pk_fp8_f32 v159, v92, v96 op_sel:[0,0,1]
	v_cvt_pk_fp8_f32 v160, v108, v112 op_sel:[0,0,1]
	v_cvt_pk_fp8_f32 v161, v124, v128 op_sel:[0,0,1]
	v_cvt_pk_fp8_f32 v162, v77, v81 op_sel:[0,0,1]
	v_cvt_pk_fp8_f32 v163, v93, v97 op_sel:[0,0,1]
	v_cvt_pk_fp8_f32 v164, v109, v113 op_sel:[0,0,1]
	v_cvt_pk_fp8_f32 v165, v125, v129 op_sel:[0,0,1]
	s_nop 1
	global_store_dwordx4 v146, v[150:153], s[18:19]
	global_store_dwordx4 v147, v[154:157], s[18:19]
	global_store_dwordx4 v148, v[158:161], s[18:19]
	global_store_dwordx4 v149, v[162:165], s[18:19]
	s_add_u32 s6, s6, s7
	s_cmpk_lt_u32 s6, 0x7000
	s_cbranch_scc0 .Lcv17_tailA
	s_lshr_b32 s8, s6, 6
	s_and_b32 s9, s6, 63
	s_lshl_b32 s10, s8, 20
	s_lshl_b32 s11, s9, 7
	s_add_u32 s10, s10, s11
	s_add_u32 s2, s12, s10
	s_addc_u32 s3, s13, 0
	s_mul_i32 s10, s8, 0x4925
	s_lshr_b32 s10, s10, 20
	s_mul_i32 s11, s10, 56
	s_sub_u32 s8, s8, s11
	s_mul_i32 s10, s10, 0xe00000
	s_lshl_b32 s8, s8, 7
	s_add_u32 s10, s10, s8
	s_mul_i32 s9, s9, 0x38000
	s_add_u32 s10, s10, s9
	s_add_u32 s18, s14, s10
	s_addc_u32 s19, s15, 0
	global_load_dwordx4 v[66:69], v130, s[2:3]
	global_load_dwordx4 v[70:73], v131, s[2:3]
	global_load_dwordx4 v[74:77], v132, s[2:3]
	global_load_dwordx4 v[78:81], v133, s[2:3]
	global_load_dwordx4 v[82:85], v134, s[2:3]
	global_load_dwordx4 v[86:89], v135, s[2:3]
	global_load_dwordx4 v[90:93], v136, s[2:3]
	global_load_dwordx4 v[94:97], v137, s[2:3]
	global_load_dwordx4 v[98:101], v138, s[2:3]
	global_load_dwordx4 v[102:105], v139, s[2:3]
	global_load_dwordx4 v[106:109], v140, s[2:3]
	global_load_dwordx4 v[110:113], v141, s[2:3]
	global_load_dwordx4 v[114:117], v142, s[2:3]
	global_load_dwordx4 v[118:121], v143, s[2:3]
	global_load_dwordx4 v[122:125], v144, s[2:3]
	global_load_dwordx4 v[126:129], v145, s[2:3]
	s_waitcnt vmcnt(20)
	v_mul_f32_e32 v2, s16, v2
	v_mul_f32_e32 v3, s16, v3
	v_mul_f32_e32 v4, s16, v4
	v_mul_f32_e32 v5, s16, v5
	v_mul_f32_e32 v6, s16, v6
	v_mul_f32_e32 v7, s16, v7
	v_mul_f32_e32 v8, s16, v8
	v_mul_f32_e32 v9, s16, v9
	v_mul_f32_e32 v10, s16, v10
	v_mul_f32_e32 v11, s16, v11
	v_mul_f32_e32 v12, s16, v12
	v_mul_f32_e32 v13, s16, v13
	v_mul_f32_e32 v14, s16, v14
	v_mul_f32_e32 v15, s16, v15
	v_mul_f32_e32 v16, s16, v16
	v_mul_f32_e32 v17, s16, v17
	v_mul_f32_e32 v18, s16, v18
	v_mul_f32_e32 v19, s16, v19
	v_mul_f32_e32 v20, s16, v20
	v_mul_f32_e32 v21, s16, v21
	v_mul_f32_e32 v22, s16, v22
	v_mul_f32_e32 v23, s16, v23
	v_mul_f32_e32 v24, s16, v24
	v_mul_f32_e32 v25, s16, v25
	v_mul_f32_e32 v26, s16, v26
	v_mul_f32_e32 v27, s16, v27
	v_mul_f32_e32 v28, s16, v28
	v_mul_f32_e32 v29, s16, v29
	v_mul_f32_e32 v30, s16, v30
	v_mul_f32_e32 v31, s16, v31
	v_mul_f32_e32 v32, s16, v32
	v_mul_f32_e32 v33, s16, v33
	v_mul_f32_e32 v34, s16, v34
	v_mul_f32_e32 v35, s16, v35
	v_mul_f32_e32 v36, s16, v36
	v_mul_f32_e32 v37, s16, v37
	v_mul_f32_e32 v38, s16, v38
	v_mul_f32_e32 v39, s16, v39
	v_mul_f32_e32 v40, s16, v40
	v_mul_f32_e32 v41, s16, v41
	v_mul_f32_e32 v42, s16, v42
	v_mul_f32_e32 v43, s16, v43
	v_mul_f32_e32 v44, s16, v44
	v_mul_f32_e32 v45, s16, v45
	v_mul_f32_e32 v46, s16, v46
	v_mul_f32_e32 v47, s16, v47
	v_mul_f32_e32 v48, s16, v48
	v_mul_f32_e32 v49, s16, v49
	v_mul_f32_e32 v50, s16, v50
	v_mul_f32_e32 v51, s16, v51
	v_mul_f32_e32 v52, s16, v52
	v_mul_f32_e32 v53, s16, v53
	v_mul_f32_e32 v54, s16, v54
	v_mul_f32_e32 v55, s16, v55
	v_mul_f32_e32 v56, s16, v56
	v_mul_f32_e32 v57, s16, v57
	v_mul_f32_e32 v58, s16, v58
	v_mul_f32_e32 v59, s16, v59
	v_mul_f32_e32 v60, s16, v60
	v_mul_f32_e32 v61, s16, v61
	v_mul_f32_e32 v62, s16, v62
	v_mul_f32_e32 v63, s16, v63
	v_mul_f32_e32 v64, s16, v64
	v_mul_f32_e32 v65, s16, v65
	v_cvt_pk_fp8_f32 v150, v2, v6
	v_cvt_pk_fp8_f32 v151, v18, v22
	v_cvt_pk_fp8_f32 v152, v34, v38
	v_cvt_pk_fp8_f32 v153, v50, v54
	v_cvt_pk_fp8_f32 v154, v3, v7
	v_cvt_pk_fp8_f32 v155, v19, v23
	v_cvt_pk_fp8_f32 v156, v35, v39
	v_cvt_pk_fp8_f32 v157, v51, v55
	v_cvt_pk_fp8_f32 v158, v4, v8
	v_cvt_pk_fp8_f32 v159, v20, v24
	v_cvt_pk_fp8_f32 v160, v36, v40
	v_cvt_pk_fp8_f32 v161, v52, v56
	v_cvt_pk_fp8_f32 v162, v5, v9
	v_cvt_pk_fp8_f32 v163, v21, v25
	v_cvt_pk_fp8_f32 v164, v37, v41
	v_cvt_pk_fp8_f32 v165, v53, v57
	v_cvt_pk_fp8_f32 v150, v10, v14 op_sel:[0,0,1]
	v_cvt_pk_fp8_f32 v151, v26, v30 op_sel:[0,0,1]
	v_cvt_pk_fp8_f32 v152, v42, v46 op_sel:[0,0,1]
	v_cvt_pk_fp8_f32 v153, v58, v62 op_sel:[0,0,1]
	v_cvt_pk_fp8_f32 v154, v11, v15 op_sel:[0,0,1]
	v_cvt_pk_fp8_f32 v155, v27, v31 op_sel:[0,0,1]
	v_cvt_pk_fp8_f32 v156, v43, v47 op_sel:[0,0,1]
	v_cvt_pk_fp8_f32 v157, v59, v63 op_sel:[0,0,1]
	v_cvt_pk_fp8_f32 v158, v12, v16 op_sel:[0,0,1]
	v_cvt_pk_fp8_f32 v159, v28, v32 op_sel:[0,0,1]
	v_cvt_pk_fp8_f32 v160, v44, v48 op_sel:[0,0,1]
	v_cvt_pk_fp8_f32 v161, v60, v64 op_sel:[0,0,1]
	v_cvt_pk_fp8_f32 v162, v13, v17 op_sel:[0,0,1]
	v_cvt_pk_fp8_f32 v163, v29, v33 op_sel:[0,0,1]
	v_cvt_pk_fp8_f32 v164, v45, v49 op_sel:[0,0,1]
	v_cvt_pk_fp8_f32 v165, v61, v65 op_sel:[0,0,1]
	s_nop 1
	global_store_dwordx4 v146, v[150:153], s[4:5]
	global_store_dwordx4 v147, v[154:157], s[4:5]
	global_store_dwordx4 v148, v[158:161], s[4:5]
	global_store_dwordx4 v149, v[162:165], s[4:5]
	s_branch .Lcv17_loop
.Lcv17_tailB:
	s_waitcnt vmcnt(0)
	v_mul_f32_e32 v66, s16, v66
	v_mul_f32_e32 v67, s16, v67
	v_mul_f32_e32 v68, s16, v68
	v_mul_f32_e32 v69, s16, v69
	v_mul_f32_e32 v70, s16, v70
	v_mul_f32_e32 v71, s16, v71
	v_mul_f32_e32 v72, s16, v72
	v_mul_f32_e32 v73, s16, v73
	v_mul_f32_e32 v74, s16, v74
	v_mul_f32_e32 v75, s16, v75
	v_mul_f32_e32 v76, s16, v76
	v_mul_f32_e32 v77, s16, v77
	v_mul_f32_e32 v78, s16, v78
	v_mul_f32_e32 v79, s16, v79
	v_mul_f32_e32 v80, s16, v80
	v_mul_f32_e32 v81, s16, v81
	v_mul_f32_e32 v82, s16, v82
	v_mul_f32_e32 v83, s16, v83
	v_mul_f32_e32 v84, s16, v84
	v_mul_f32_e32 v85, s16, v85
	v_mul_f32_e32 v86, s16, v86
	v_mul_f32_e32 v87, s16, v87
	v_mul_f32_e32 v88, s16, v88
	v_mul_f32_e32 v89, s16, v89
	v_mul_f32_e32 v90, s16, v90
	v_mul_f32_e32 v91, s16, v91
	v_mul_f32_e32 v92, s16, v92
	v_mul_f32_e32 v93, s16, v93
	v_mul_f32_e32 v94, s16, v94
	v_mul_f32_e32 v95, s16, v95
	v_mul_f32_e32 v96, s16, v96
	v_mul_f32_e32 v97, s16, v97
	v_mul_f32_e32 v98, s16, v98
	v_mul_f32_e32 v99, s16, v99
	v_mul_f32_e32 v100, s16, v100
	v_mul_f32_e32 v101, s16, v101
	v_mul_f32_e32 v102, s16, v102
	v_mul_f32_e32 v103, s16, v103
	v_mul_f32_e32 v104, s16, v104
	v_mul_f32_e32 v105, s16, v105
	v_mul_f32_e32 v106, s16, v106
	v_mul_f32_e32 v107, s16, v107
	v_mul_f32_e32 v108, s16, v108
	v_mul_f32_e32 v109, s16, v109
	v_mul_f32_e32 v110, s16, v110
	v_mul_f32_e32 v111, s16, v111
	v_mul_f32_e32 v112, s16, v112
	v_mul_f32_e32 v113, s16, v113
	v_mul_f32_e32 v114, s16, v114
	v_mul_f32_e32 v115, s16, v115
	v_mul_f32_e32 v116, s16, v116
	v_mul_f32_e32 v117, s16, v117
	v_mul_f32_e32 v118, s16, v118
	v_mul_f32_e32 v119, s16, v119
	v_mul_f32_e32 v120, s16, v120
	v_mul_f32_e32 v121, s16, v121
	v_mul_f32_e32 v122, s16, v122
	v_mul_f32_e32 v123, s16, v123
	v_mul_f32_e32 v124, s16, v124
	v_mul_f32_e32 v125, s16, v125
	v_mul_f32_e32 v126, s16, v126
	v_mul_f32_e32 v127, s16, v127
	v_mul_f32_e32 v128, s16, v128
	v_mul_f32_e32 v129, s16, v129
	v_cvt_pk_fp8_f32 v150, v66, v70
	v_cvt_pk_fp8_f32 v151, v82, v86
	v_cvt_pk_fp8_f32 v152, v98, v102
	v_cvt_pk_fp8_f32 v153, v114, v118
	v_cvt_pk_fp8_f32 v154, v67, v71
	v_cvt_pk_fp8_f32 v155, v83, v87
	v_cvt_pk_fp8_f32 v156, v99, v103
	v_cvt_pk_fp8_f32 v157, v115, v119
	v_cvt_pk_fp8_f32 v158, v68, v72
	v_cvt_pk_fp8_f32 v159, v84, v88
	v_cvt_pk_fp8_f32 v160, v100, v104
	v_cvt_pk_fp8_f32 v161, v116, v120
	v_cvt_pk_fp8_f32 v162, v69, v73
	v_cvt_pk_fp8_f32 v163, v85, v89
	v_cvt_pk_fp8_f32 v164, v101, v105
	v_cvt_pk_fp8_f32 v165, v117, v121
	v_cvt_pk_fp8_f32 v150, v74, v78 op_sel:[0,0,1]
	v_cvt_pk_fp8_f32 v151, v90, v94 op_sel:[0,0,1]
	v_cvt_pk_fp8_f32 v152, v106, v110 op_sel:[0,0,1]
	v_cvt_pk_fp8_f32 v153, v122, v126 op_sel:[0,0,1]
	v_cvt_pk_fp8_f32 v154, v75, v79 op_sel:[0,0,1]
	v_cvt_pk_fp8_f32 v155, v91, v95 op_sel:[0,0,1]
	v_cvt_pk_fp8_f32 v156, v107, v111 op_sel:[0,0,1]
	v_cvt_pk_fp8_f32 v157, v123, v127 op_sel:[0,0,1]
	v_cvt_pk_fp8_f32 v158, v76, v80 op_sel:[0,0,1]
	v_cvt_pk_fp8_f32 v159, v92, v96 op_sel:[0,0,1]
	v_cvt_pk_fp8_f32 v160, v108, v112 op_sel:[0,0,1]
	v_cvt_pk_fp8_f32 v161, v124, v128 op_sel:[0,0,1]
	v_cvt_pk_fp8_f32 v162, v77, v81 op_sel:[0,0,1]
	v_cvt_pk_fp8_f32 v163, v93, v97 op_sel:[0,0,1]
	v_cvt_pk_fp8_f32 v164, v109, v113 op_sel:[0,0,1]
	v_cvt_pk_fp8_f32 v165, v125, v129 op_sel:[0,0,1]
	s_nop 1
	global_store_dwordx4 v146, v[150:153], s[18:19]
	global_store_dwordx4 v147, v[154:157], s[18:19]
	global_store_dwordx4 v148, v[158:161], s[18:19]
	global_store_dwordx4 v149, v[162:165], s[18:19]
	s_branch .Lcv17_done
.Lcv17_tailA:
	s_waitcnt vmcnt(0)
	v_mul_f32_e32 v2, s16, v2
	v_mul_f32_e32 v3, s16, v3
	v_mul_f32_e32 v4, s16, v4
	v_mul_f32_e32 v5, s16, v5
	v_mul_f32_e32 v6, s16, v6
	v_mul_f32_e32 v7, s16, v7
	v_mul_f32_e32 v8, s16, v8
	v_mul_f32_e32 v9, s16, v9
	v_mul_f32_e32 v10, s16, v10
	v_mul_f32_e32 v11, s16, v11
	v_mul_f32_e32 v12, s16, v12
	v_mul_f32_e32 v13, s16, v13
	v_mul_f32_e32 v14, s16, v14
	v_mul_f32_e32 v15, s16, v15
	v_mul_f32_e32 v16, s16, v16
	v_mul_f32_e32 v17, s16, v17
	v_mul_f32_e32 v18, s16, v18
	v_mul_f32_e32 v19, s16, v19
	v_mul_f32_e32 v20, s16, v20
	v_mul_f32_e32 v21, s16, v21
	v_mul_f32_e32 v22, s16, v22
	v_mul_f32_e32 v23, s16, v23
	v_mul_f32_e32 v24, s16, v24
	v_mul_f32_e32 v25, s16, v25
	v_mul_f32_e32 v26, s16, v26
	v_mul_f32_e32 v27, s16, v27
	v_mul_f32_e32 v28, s16, v28
	v_mul_f32_e32 v29, s16, v29
	v_mul_f32_e32 v30, s16, v30
	v_mul_f32_e32 v31, s16, v31
	v_mul_f32_e32 v32, s16, v32
	v_mul_f32_e32 v33, s16, v33
	v_mul_f32_e32 v34, s16, v34
	v_mul_f32_e32 v35, s16, v35
	v_mul_f32_e32 v36, s16, v36
	v_mul_f32_e32 v37, s16, v37
	v_mul_f32_e32 v38, s16, v38
	v_mul_f32_e32 v39, s16, v39
	v_mul_f32_e32 v40, s16, v40
	v_mul_f32_e32 v41, s16, v41
	v_mul_f32_e32 v42, s16, v42
	v_mul_f32_e32 v43, s16, v43
	v_mul_f32_e32 v44, s16, v44
	v_mul_f32_e32 v45, s16, v45
	v_mul_f32_e32 v46, s16, v46
	v_mul_f32_e32 v47, s16, v47
	v_mul_f32_e32 v48, s16, v48
	v_mul_f32_e32 v49, s16, v49
	v_mul_f32_e32 v50, s16, v50
	v_mul_f32_e32 v51, s16, v51
	v_mul_f32_e32 v52, s16, v52
	v_mul_f32_e32 v53, s16, v53
	v_mul_f32_e32 v54, s16, v54
	v_mul_f32_e32 v55, s16, v55
	v_mul_f32_e32 v56, s16, v56
	v_mul_f32_e32 v57, s16, v57
	v_mul_f32_e32 v58, s16, v58
	v_mul_f32_e32 v59, s16, v59
	v_mul_f32_e32 v60, s16, v60
	v_mul_f32_e32 v61, s16, v61
	v_mul_f32_e32 v62, s16, v62
	v_mul_f32_e32 v63, s16, v63
	v_mul_f32_e32 v64, s16, v64
	v_mul_f32_e32 v65, s16, v65
	v_cvt_pk_fp8_f32 v150, v2, v6
	v_cvt_pk_fp8_f32 v151, v18, v22
	v_cvt_pk_fp8_f32 v152, v34, v38
	v_cvt_pk_fp8_f32 v153, v50, v54
	v_cvt_pk_fp8_f32 v154, v3, v7
	v_cvt_pk_fp8_f32 v155, v19, v23
	v_cvt_pk_fp8_f32 v156, v35, v39
	v_cvt_pk_fp8_f32 v157, v51, v55
	v_cvt_pk_fp8_f32 v158, v4, v8
	v_cvt_pk_fp8_f32 v159, v20, v24
	v_cvt_pk_fp8_f32 v160, v36, v40
	v_cvt_pk_fp8_f32 v161, v52, v56
	v_cvt_pk_fp8_f32 v162, v5, v9
	v_cvt_pk_fp8_f32 v163, v21, v25
	v_cvt_pk_fp8_f32 v164, v37, v41
	v_cvt_pk_fp8_f32 v165, v53, v57
	v_cvt_pk_fp8_f32 v150, v10, v14 op_sel:[0,0,1]
	v_cvt_pk_fp8_f32 v151, v26, v30 op_sel:[0,0,1]
	v_cvt_pk_fp8_f32 v152, v42, v46 op_sel:[0,0,1]
	v_cvt_pk_fp8_f32 v153, v58, v62 op_sel:[0,0,1]
	v_cvt_pk_fp8_f32 v154, v11, v15 op_sel:[0,0,1]
	v_cvt_pk_fp8_f32 v155, v27, v31 op_sel:[0,0,1]
	v_cvt_pk_fp8_f32 v156, v43, v47 op_sel:[0,0,1]
	v_cvt_pk_fp8_f32 v157, v59, v63 op_sel:[0,0,1]
	v_cvt_pk_fp8_f32 v158, v12, v16 op_sel:[0,0,1]
	v_cvt_pk_fp8_f32 v159, v28, v32 op_sel:[0,0,1]
	v_cvt_pk_fp8_f32 v160, v44, v48 op_sel:[0,0,1]
	v_cvt_pk_fp8_f32 v161, v60, v64 op_sel:[0,0,1]
	v_cvt_pk_fp8_f32 v162, v13, v17 op_sel:[0,0,1]
	v_cvt_pk_fp8_f32 v163, v29, v33 op_sel:[0,0,1]
	v_cvt_pk_fp8_f32 v164, v45, v49 op_sel:[0,0,1]
	v_cvt_pk_fp8_f32 v165, v61, v65 op_sel:[0,0,1]
	s_nop 1
	global_store_dwordx4 v146, v[150:153], s[4:5]
	global_store_dwordx4 v147, v[154:157], s[4:5]
	global_store_dwordx4 v148, v[158:161], s[4:5]
	global_store_dwordx4 v149, v[162:165], s[4:5]
.Lcv17_done:
	s_waitcnt vmcnt(0)
	s_cmp_eq_u32 s17, 0
	s_cbranch_scc1 .LBB0_1731
	s_branch .Lcv17_gemm
.Lcv17_gemm:
	v_mov_b32_e32 v1, 0x8000
	global_load_dword v2, v1, s[78:79] sc1
	global_load_dword v3, v1, s[78:79] offset:256 sc1
	global_load_dword v4, v1, s[78:79] offset:512 sc1
	global_load_dword v5, v1, s[78:79] offset:768 sc1
	global_load_dword v6, v1, s[78:79] offset:1024 sc1
	global_load_dword v7, v1, s[78:79] offset:1280 sc1
	global_load_dword v8, v1, s[78:79] offset:1536 sc1
	global_load_dword v9, v1, s[78:79] offset:1792 sc1
	v_mov_b32_e32 v1, 0x5cba0000
	global_load_dword v1, v1, s[78:79] offset:4
	s_and_b32 s4, s97, 7
	v_readfirstlane_b32 s3, v0
	s_waitcnt vmcnt(0)
	v_readfirstlane_b32 s10, v2
	v_readfirstlane_b32 s2, v3
	v_readfirstlane_b32 s5, v4
	v_readfirstlane_b32 s6, v5
	s_addk_i32 s10, 0xff
	s_addk_i32 s2, 0xff
	s_addk_i32 s5, 0xff
	v_readfirstlane_b32 s11, v9
	s_addk_i32 s6, 0xff
	s_addk_i32 s11, 0xff
	s_and_b32 s12, s10, 0xffffff00
	s_and_b32 s2, s2, 0xffffff00
	v_readfirstlane_b32 s7, v6
	s_and_b32 s5, s5, 0xffffff00
	s_and_b32 s13, s6, 0xffffff00
	s_and_b32 s6, s11, 0xffffff00
	s_add_i32 s11, s2, s12
	v_readfirstlane_b32 s8, v7
	s_addk_i32 s7, 0xff
	s_add_i32 s12, s5, s11
	v_readfirstlane_b32 s9, v8
	s_addk_i32 s8, 0xff
	s_and_b32 s14, s7, 0xffffff00
	s_add_i32 s13, s13, s12
	s_addk_i32 s9, 0xff
	s_and_b32 s15, s8, 0xffffff00
	s_add_i32 s14, s14, s13
	s_and_b32 s16, s9, 0xffffff00
	s_add_i32 s15, s15, s14
	s_add_i32 s16, s16, s15
	s_add_i32 s6, s6, s16
	s_ashr_i32 s33, s6, 8
	s_cmp_lg_u32 s4, 0
	s_cselect_b64 s[4:5], -1, 0
	s_mul_i32 s2, s33, 56
	s_and_b64 vcc, exec, s[4:5]
	s_cbranch_vccz .LBB0_1743
	s_ashr_i32 s75, s74, 31
	s_cmp_lt_i32 s74, s2
	s_cselect_b64 s[6:7], -1, 0
	s_mov_b64 s[22:23], s[74:75]
	s_cbranch_execnz .LBB0_1711

.LBB0_1714:
	s_add_i32 s83, s24, s25
	v_readlane_b32 s24, v251, 9
	v_readlane_b32 s26, v251, 11
	v_readlane_b32 s25, v251, 10
	v_readlane_b32 s27, v251, 12
	s_add_u32 s24, s26, 0x5cbc0000
	s_addc_u32 s25, s27, 0
	s_add_u32 s26, s26, 0x3e500000
	s_addc_u32 s27, s27, 0
	s_lshl_b32 s28, s28, 5
	s_and_b32 s38, s28, 0x60
	s_mov_b64 s[28:29], 0x80
	s_add_i32 m0, s47, 0x18000
	v_lshl_add_u64 v[8:9], v[8:9], 0, s[28:29]
	s_lshl_b32 s31, s30, 13
	s_lshl_b32 s36, s38, 7
	s_waitcnt vmcnt(2)
	s_barrier
	global_load_lds_dwordx4 v[8:9], off
	v_lshl_add_u64 v[6:7], v[6:7], 0, s[28:29]
	s_add_i32 m0, s47, 0x1a000
	s_add_i32 s71, s47, 0x8000
	s_add_i32 s72, s47, 0xa000
	global_load_lds_dwordx4 v[6:7], off
	v_lshl_add_u64 v[2:3], v[2:3], 0, s[28:29]
	s_mov_b32 m0, s71
	s_add_u32 s34, s52, 0x40080
	global_load_lds_dwordx4 v[2:3], off
	v_lshl_add_u64 v[2:3], v[4:5], 0, s[28:29]
	s_mov_b32 m0, s72
	s_addc_u32 s35, s53, 0
	global_load_lds_dwordx4 v[2:3], off
	s_add_i32 m0, s47, 0x1c000
	v_lshl_add_u64 v[2:3], s[34:35], 0, v[164:165]
	global_load_lds_dwordx4 v[2:3], off
	v_lshl_add_u64 v[2:3], s[34:35], 0, v[168:169]
	s_add_i32 m0, s47, 0x1e000
	v_and_b32_e32 v4, 32, v180
	global_load_lds_dwordx4 v[2:3], off
	v_and_b32_e32 v2, 15, v0
	v_lshlrev_b32_e32 v3, 1, v13
	v_lshl_or_b32 v179, s30, 6, v2
	v_lshl_or_b32 v2, v2, 6, v3
	v_lshlrev_b32_e32 v5, 6, v0
	s_movk_i32 s30, 0x3c0
	s_cmpk_lt_u32 s3, 0x100
	s_mov_b32 s34, s74
	v_bitop3_b32 v2, v2, s31, v4 bitop3:0xde
	v_and_or_b32 v3, v5, s30, v3
	s_cselect_b64 s[30:31], -1, 0
	s_and_b32 s39, s34, 7
	s_waitcnt lgkmcnt(0)
	v_bitop3_b32 v181, s36, v3, v4 bitop3:0xf6
	s_mov_b32 s92, s34
	s_ashr_i32 s40, s34, 3
	s_mul_hi_i32 s35, s39, s2
	s_mul_i32 s34, s39, s2
	v_lshlrev_b32_e32 v3, 8, v0
	s_ashr_i64 s[36:37], s[34:35], 3
	s_add_i32 s34, s39, 1
	v_and_b32_e32 v3, 0x18000, v3
	v_lshlrev_b32_e32 v4, 11, v12
	s_ashr_i32 s75, s97, 3
	s_cmp_eq_u32 s97, 0x100
	s_cselect_b32 s76, 4, 0
	s_sub_i32 s75, s75, s76
	s_mul_hi_i32 s35, s34, s2
	s_mul_i32 s34, s34, s2
	v_or3_b32 v3, v10, v3, v4
	s_ashr_i32 s73, s97, 31
	s_ashr_i32 s74, s74, 31
	s_ashr_i32 s3, s2, 31
	s_ashr_i64 s[34:35], s[34:35], 3
	s_ashr_i32 s76, s75, 31
	s_ashr_i32 s39, s40, 31
	v_add_u32_e32 v170, v3, v11
	v_lshlrev_b32_e32 v3, 4, v14
	s_waitcnt vmcnt(6)
	s_add_u32 s77, s36, s40
	v_and_b32_e32 v3, 0x38000, v3
	s_addc_u32 s78, s37, s39
	v_or3_b32 v3, v10, v3, v4
	s_add_i32 s79, 0, 0x10000
	s_add_i32 s80, 0, 0x14000
	v_or_b32_e32 v186, s38, v13
	v_mov_b32_e32 v171, v165
	v_add_u32_e32 v172, v3, v11
	v_mov_b32_e32 v173, v165
	v_add_u32_e32 v187, s79, v181
	v_add_u32_e32 v188, s80, v181
	v_add_u32_e32 v189, 0, v2
	s_movk_i32 s81, 0x1c00
	s_barrier
	s_branch .LBB0_1717
